# forget-weight gather in one round trip; s_setprio toggles removed from GEMM loops (third measurement)
# speedup vs baseline: 1.0130x; 1.0130x over previous
.LBB0_114:
	ds_read_b128 v[130:133], v220
	ds_read_b128 v[134:137], v220 offset:1024
	ds_read_b128 v[138:141], v220 offset:2048
	ds_read_b128 v[142:145], v220 offset:3072
	ds_read_b128 v[146:149], v221
	ds_read_b128 v[150:153], v221 offset:1024
	ds_read_b128 v[154:157], v221 offset:2048
	ds_read_b128 v[158:161], v221 offset:3072
	s_add_i32 s46, s64, 0xfff80080
	s_cmp_eq_u32 s84, 28
	s_cselect_b32 s87, s62, s46
	s_cselect_b32 s86, s63, s65
	s_or_b32 s85, s87, 0x80
	s_mov_b32 m0, s93
	ds_read_b128 v[162:165], v222
	ds_read_b128 v[166:169], v222 offset:1024
	ds_read_b128 v[170:173], v222 offset:2048
	ds_read_b128 v[174:177], v222 offset:3072
	ds_read_b128 v[178:181], v222 offset:4096
	ds_read_b128 v[182:185], v222 offset:5120
	ds_read_b128 v[186:189], v222 offset:6144
	ds_read_b128 v[212:215], v222 offset:7168
	buffer_load_dwordx4 v1, s[40:43], s64 offen lds
	s_mov_b32 m0, s94
	s_nop 0
	buffer_load_dwordx4 v216, s[40:43], s64 offen lds
	s_waitcnt vmcnt(8)
	s_waitcnt lgkmcnt(0)
	s_barrier
	s_waitcnt lgkmcnt(7)
	v_mfma_f32_16x16x32_bf16 v[126:129], v[130:133], v[162:165], v[126:129]
	v_mfma_f32_16x16x32_bf16 v[122:125], v[138:141], v[162:165], v[122:125]
	s_waitcnt lgkmcnt(5)
	v_mfma_f32_16x16x32_bf16 v[114:117], v[130:133], v[170:173], v[114:117]
	v_mfma_f32_16x16x32_bf16 v[106:109], v[138:141], v[170:173], v[106:109]
	s_waitcnt lgkmcnt(3)
	v_mfma_f32_16x16x32_bf16 v[102:105], v[130:133], v[178:181], v[102:105]
	v_mfma_f32_16x16x32_bf16 v[94:97], v[138:141], v[178:181], v[94:97]
	s_waitcnt lgkmcnt(1)
	v_mfma_f32_16x16x32_bf16 v[86:89], v[130:133], v[186:189], v[86:89]
	v_mfma_f32_16x16x32_bf16 v[78:81], v[138:141], v[186:189], v[78:81]
	v_mfma_f32_16x16x32_bf16 v[126:129], v[134:137], v[166:169], v[126:129]
	v_mfma_f32_16x16x32_bf16 v[122:125], v[142:145], v[166:169], v[122:125]
	v_mfma_f32_16x16x32_bf16 v[114:117], v[134:137], v[174:177], v[114:117]
	v_mfma_f32_16x16x32_bf16 v[106:109], v[142:145], v[174:177], v[106:109]
	v_mfma_f32_16x16x32_bf16 v[102:105], v[134:137], v[182:185], v[102:105]
	v_mfma_f32_16x16x32_bf16 v[94:97], v[142:145], v[182:185], v[94:97]
	s_waitcnt lgkmcnt(0)
	v_mfma_f32_16x16x32_bf16 v[86:89], v[134:137], v[212:215], v[86:89]
	v_mfma_f32_16x16x32_bf16 v[78:81], v[142:145], v[212:215], v[78:81]
	v_mfma_f32_16x16x32_bf16 v[118:121], v[146:149], v[162:165], v[118:121]
	v_mfma_f32_16x16x32_bf16 v[110:113], v[154:157], v[162:165], v[110:113]
	v_mfma_f32_16x16x32_bf16 v[98:101], v[146:149], v[170:173], v[98:101]
	v_mfma_f32_16x16x32_bf16 v[90:93], v[154:157], v[170:173], v[90:93]
	v_mfma_f32_16x16x32_bf16 v[82:85], v[146:149], v[178:181], v[82:85]
	v_mfma_f32_16x16x32_bf16 v[74:77], v[154:157], v[178:181], v[74:77]
	v_mfma_f32_16x16x32_bf16 v[70:73], v[146:149], v[186:189], v[70:73]
	v_mfma_f32_16x16x32_bf16 v[66:69], v[154:157], v[186:189], v[66:69]
	v_mfma_f32_16x16x32_bf16 v[118:121], v[150:153], v[166:169], v[118:121]
	v_mfma_f32_16x16x32_bf16 v[110:113], v[158:161], v[166:169], v[110:113]
	v_mfma_f32_16x16x32_bf16 v[98:101], v[150:153], v[174:177], v[98:101]
	v_mfma_f32_16x16x32_bf16 v[90:93], v[158:161], v[174:177], v[90:93]
	v_mfma_f32_16x16x32_bf16 v[82:85], v[150:153], v[182:185], v[82:85]
	v_mfma_f32_16x16x32_bf16 v[74:77], v[158:161], v[182:185], v[74:77]
	v_mfma_f32_16x16x32_bf16 v[70:73], v[150:153], v[212:215], v[70:73]
	v_mfma_f32_16x16x32_bf16 v[66:69], v[158:161], v[212:215], v[66:69]
	s_barrier
	s_mov_b32 m0, s69
	s_mov_b32 s46, s42
	s_mov_b32 s47, s43
	ds_read_b128 v[162:165], v222 offset:16384
	ds_read_b128 v[166:169], v222 offset:17408
	ds_read_b128 v[170:173], v222 offset:18432
	ds_read_b128 v[174:177], v222 offset:19456
	ds_read_b128 v[178:181], v222 offset:20480
	ds_read_b128 v[182:185], v222 offset:21504
	ds_read_b128 v[186:189], v222 offset:22528
	ds_read_b128 v[212:215], v222 offset:23552
	buffer_load_dwordx4 v191, s[44:47], s86 offen lds
	s_mov_b32 m0, s70
	s_add_i32 s88, s86, 0x80000
	buffer_load_dwordx4 v217, s[44:47], s86 offen lds
	s_mov_b32 m0, s71
	s_nop 0
	buffer_load_dwordx4 v191, s[44:47], s88 offen lds
	s_mov_b32 m0, s72
	s_nop 0
	buffer_load_dwordx4 v217, s[44:47], s88 offen lds
	s_mov_b32 m0, s68
	s_nop 0
	buffer_load_dwordx4 v1, s[40:43], s87 offen lds
	s_mov_b32 m0, s73
	s_nop 0
	buffer_load_dwordx4 v216, s[40:43], s87 offen lds
	s_waitcnt vmcnt(8)
	s_waitcnt lgkmcnt(0)
	s_barrier
	s_waitcnt lgkmcnt(7)
	v_mfma_f32_16x16x32_bf16 v[62:65], v[130:133], v[162:165], v[62:65]
	v_mfma_f32_16x16x32_bf16 v[58:61], v[138:141], v[162:165], v[58:61]
	s_waitcnt lgkmcnt(5)
	v_mfma_f32_16x16x32_bf16 v[54:57], v[130:133], v[170:173], v[54:57]
	v_mfma_f32_16x16x32_bf16 v[46:49], v[138:141], v[170:173], v[46:49]
	s_waitcnt lgkmcnt(3)
	v_mfma_f32_16x16x32_bf16 v[38:41], v[130:133], v[178:181], v[38:41]
	v_mfma_f32_16x16x32_bf16 v[30:33], v[138:141], v[178:181], v[30:33]
	s_waitcnt lgkmcnt(1)
	v_mfma_f32_16x16x32_bf16 v[22:25], v[130:133], v[186:189], v[22:25]
	v_mfma_f32_16x16x32_bf16 v[14:17], v[138:141], v[186:189], v[14:17]
	v_mfma_f32_16x16x32_bf16 v[62:65], v[134:137], v[166:169], v[62:65]
	v_mfma_f32_16x16x32_bf16 v[58:61], v[142:145], v[166:169], v[58:61]
	v_mfma_f32_16x16x32_bf16 v[54:57], v[134:137], v[174:177], v[54:57]
	v_mfma_f32_16x16x32_bf16 v[46:49], v[142:145], v[174:177], v[46:49]
	v_mfma_f32_16x16x32_bf16 v[38:41], v[134:137], v[182:185], v[38:41]
	v_mfma_f32_16x16x32_bf16 v[30:33], v[142:145], v[182:185], v[30:33]
	s_waitcnt lgkmcnt(0)
	v_mfma_f32_16x16x32_bf16 v[22:25], v[134:137], v[212:215], v[22:25]
	v_mfma_f32_16x16x32_bf16 v[14:17], v[142:145], v[212:215], v[14:17]
	v_mfma_f32_16x16x32_bf16 v[50:53], v[146:149], v[162:165], v[50:53]
	v_mfma_f32_16x16x32_bf16 v[42:45], v[154:157], v[162:165], v[42:45]
	v_mfma_f32_16x16x32_bf16 v[34:37], v[146:149], v[170:173], v[34:37]
	v_mfma_f32_16x16x32_bf16 v[26:29], v[154:157], v[170:173], v[26:29]
	v_mfma_f32_16x16x32_bf16 v[18:21], v[146:149], v[178:181], v[18:21]
	v_mfma_f32_16x16x32_bf16 v[10:13], v[154:157], v[178:181], v[10:13]
	v_mfma_f32_16x16x32_bf16 v[6:9], v[146:149], v[186:189], v[6:9]
	v_mfma_f32_16x16x32_bf16 v[2:5], v[154:157], v[186:189], v[2:5]
	v_mfma_f32_16x16x32_bf16 v[50:53], v[150:153], v[166:169], v[50:53]
	v_mfma_f32_16x16x32_bf16 v[42:45], v[158:161], v[166:169], v[42:45]
	v_mfma_f32_16x16x32_bf16 v[34:37], v[150:153], v[174:177], v[34:37]
	v_mfma_f32_16x16x32_bf16 v[26:29], v[158:161], v[174:177], v[26:29]
	v_mfma_f32_16x16x32_bf16 v[18:21], v[150:153], v[182:185], v[18:21]
	v_mfma_f32_16x16x32_bf16 v[10:13], v[158:161], v[182:185], v[10:13]
	v_mfma_f32_16x16x32_bf16 v[6:9], v[150:153], v[212:215], v[6:9]
	v_mfma_f32_16x16x32_bf16 v[2:5], v[158:161], v[212:215], v[2:5]
	s_barrier
	ds_read_b128 v[130:133], v223
	ds_read_b128 v[134:137], v223 offset:1024
	ds_read_b128 v[138:141], v223 offset:2048
	ds_read_b128 v[142:145], v223 offset:3072
	ds_read_b128 v[146:149], v224
	ds_read_b128 v[150:153], v224 offset:1024
	ds_read_b128 v[154:157], v224 offset:2048
	ds_read_b128 v[158:161], v224 offset:3072
	s_add_i32 s87, s87, 0x80000
	s_mov_b32 m0, s74
	ds_read_b128 v[162:165], v222 offset:32768
	ds_read_b128 v[166:169], v222 offset:33792
	ds_read_b128 v[170:173], v222 offset:34816
	ds_read_b128 v[174:177], v222 offset:35840
	ds_read_b128 v[178:181], v222 offset:36864
	ds_read_b128 v[182:185], v222 offset:37888
	ds_read_b128 v[186:189], v222 offset:38912
	ds_read_b128 v[212:215], v222 offset:39936
	buffer_load_dwordx4 v1, s[40:43], s87 offen lds
	s_mov_b32 m0, s75
	s_nop 0
	buffer_load_dwordx4 v216, s[40:43], s87 offen lds
	s_waitcnt vmcnt(8)
	s_waitcnt lgkmcnt(0)
	s_barrier
	s_waitcnt lgkmcnt(7)
	v_mfma_f32_16x16x32_bf16 v[126:129], v[130:133], v[162:165], v[126:129]
	v_mfma_f32_16x16x32_bf16 v[122:125], v[138:141], v[162:165], v[122:125]
	s_waitcnt lgkmcnt(5)
	v_mfma_f32_16x16x32_bf16 v[114:117], v[130:133], v[170:173], v[114:117]
	v_mfma_f32_16x16x32_bf16 v[106:109], v[138:141], v[170:173], v[106:109]
	s_waitcnt lgkmcnt(3)
	v_mfma_f32_16x16x32_bf16 v[102:105], v[130:133], v[178:181], v[102:105]
	v_mfma_f32_16x16x32_bf16 v[94:97], v[138:141], v[178:181], v[94:97]
	s_waitcnt lgkmcnt(1)
	v_mfma_f32_16x16x32_bf16 v[86:89], v[130:133], v[186:189], v[86:89]
	v_mfma_f32_16x16x32_bf16 v[78:81], v[138:141], v[186:189], v[78:81]
	v_mfma_f32_16x16x32_bf16 v[126:129], v[134:137], v[166:169], v[126:129]
	v_mfma_f32_16x16x32_bf16 v[122:125], v[142:145], v[166:169], v[122:125]
	v_mfma_f32_16x16x32_bf16 v[114:117], v[134:137], v[174:177], v[114:117]
	v_mfma_f32_16x16x32_bf16 v[106:109], v[142:145], v[174:177], v[106:109]
	v_mfma_f32_16x16x32_bf16 v[102:105], v[134:137], v[182:185], v[102:105]
	v_mfma_f32_16x16x32_bf16 v[94:97], v[142:145], v[182:185], v[94:97]
	s_waitcnt lgkmcnt(0)
	v_mfma_f32_16x16x32_bf16 v[86:89], v[134:137], v[212:215], v[86:89]
	v_mfma_f32_16x16x32_bf16 v[78:81], v[142:145], v[212:215], v[78:81]
	v_mfma_f32_16x16x32_bf16 v[118:121], v[146:149], v[162:165], v[118:121]
	v_mfma_f32_16x16x32_bf16 v[110:113], v[154:157], v[162:165], v[110:113]
	v_mfma_f32_16x16x32_bf16 v[98:101], v[146:149], v[170:173], v[98:101]
	v_mfma_f32_16x16x32_bf16 v[90:93], v[154:157], v[170:173], v[90:93]
	v_mfma_f32_16x16x32_bf16 v[82:85], v[146:149], v[178:181], v[82:85]
	v_mfma_f32_16x16x32_bf16 v[74:77], v[154:157], v[178:181], v[74:77]
	v_mfma_f32_16x16x32_bf16 v[70:73], v[146:149], v[186:189], v[70:73]
	v_mfma_f32_16x16x32_bf16 v[66:69], v[154:157], v[186:189], v[66:69]
	v_mfma_f32_16x16x32_bf16 v[118:121], v[150:153], v[166:169], v[118:121]
	v_mfma_f32_16x16x32_bf16 v[110:113], v[158:161], v[166:169], v[110:113]
	v_mfma_f32_16x16x32_bf16 v[98:101], v[150:153], v[174:177], v[98:101]
	v_mfma_f32_16x16x32_bf16 v[90:93], v[158:161], v[174:177], v[90:93]
	v_mfma_f32_16x16x32_bf16 v[82:85], v[150:153], v[182:185], v[82:85]
	v_mfma_f32_16x16x32_bf16 v[74:77], v[158:161], v[182:185], v[74:77]
	v_mfma_f32_16x16x32_bf16 v[70:73], v[150:153], v[212:215], v[70:73]
	v_mfma_f32_16x16x32_bf16 v[66:69], v[158:161], v[212:215], v[66:69]
	s_barrier
	s_mov_b32 m0, s79
	s_or_b32 s87, s86, 0x80
	ds_read_b128 v[162:165], v222 offset:49152
	ds_read_b128 v[166:169], v222 offset:50176
	ds_read_b128 v[170:173], v222 offset:51200
	ds_read_b128 v[174:177], v222 offset:52224
	ds_read_b128 v[178:181], v222 offset:53248
	ds_read_b128 v[182:185], v222 offset:54272
	ds_read_b128 v[186:189], v222 offset:55296
	ds_read_b128 v[212:215], v222 offset:56320
	buffer_load_dwordx4 v191, s[44:47], s87 offen lds
	s_mov_b32 m0, s80
	s_add_i32 s86, s86, 0x80080
	buffer_load_dwordx4 v217, s[44:47], s87 offen lds
	s_mov_b32 m0, s83
	s_nop 0
	buffer_load_dwordx4 v191, s[44:47], s86 offen lds
	s_mov_b32 m0, s92
	s_nop 0
	buffer_load_dwordx4 v217, s[44:47], s86 offen lds
	s_mov_b32 m0, s81
	s_nop 0
	buffer_load_dwordx4 v1, s[40:43], s85 offen lds
	s_mov_b32 m0, s82
	s_nop 0
	buffer_load_dwordx4 v216, s[40:43], s85 offen lds
	s_waitcnt vmcnt(8)
	s_waitcnt lgkmcnt(0)
	s_barrier
	s_waitcnt lgkmcnt(7)
	v_mfma_f32_16x16x32_bf16 v[62:65], v[130:133], v[162:165], v[62:65]
	v_mfma_f32_16x16x32_bf16 v[58:61], v[138:141], v[162:165], v[58:61]
	s_waitcnt lgkmcnt(5)
	v_mfma_f32_16x16x32_bf16 v[54:57], v[130:133], v[170:173], v[54:57]
	v_mfma_f32_16x16x32_bf16 v[46:49], v[138:141], v[170:173], v[46:49]
	s_waitcnt lgkmcnt(3)
	v_mfma_f32_16x16x32_bf16 v[38:41], v[130:133], v[178:181], v[38:41]
	v_mfma_f32_16x16x32_bf16 v[30:33], v[138:141], v[178:181], v[30:33]
	s_waitcnt lgkmcnt(1)
	v_mfma_f32_16x16x32_bf16 v[22:25], v[130:133], v[186:189], v[22:25]
	v_mfma_f32_16x16x32_bf16 v[14:17], v[138:141], v[186:189], v[14:17]
	v_mfma_f32_16x16x32_bf16 v[62:65], v[134:137], v[166:169], v[62:65]
	v_mfma_f32_16x16x32_bf16 v[58:61], v[142:145], v[166:169], v[58:61]
	v_mfma_f32_16x16x32_bf16 v[54:57], v[134:137], v[174:177], v[54:57]
	v_mfma_f32_16x16x32_bf16 v[46:49], v[142:145], v[174:177], v[46:49]
	v_mfma_f32_16x16x32_bf16 v[38:41], v[134:137], v[182:185], v[38:41]
	v_mfma_f32_16x16x32_bf16 v[30:33], v[142:145], v[182:185], v[30:33]
	s_waitcnt lgkmcnt(0)
	v_mfma_f32_16x16x32_bf16 v[22:25], v[134:137], v[212:215], v[22:25]
	v_mfma_f32_16x16x32_bf16 v[14:17], v[142:145], v[212:215], v[14:17]
	v_mfma_f32_16x16x32_bf16 v[50:53], v[146:149], v[162:165], v[50:53]
	v_mfma_f32_16x16x32_bf16 v[42:45], v[154:157], v[162:165], v[42:45]
	v_mfma_f32_16x16x32_bf16 v[34:37], v[146:149], v[170:173], v[34:37]
	v_mfma_f32_16x16x32_bf16 v[26:29], v[154:157], v[170:173], v[26:29]
	v_mfma_f32_16x16x32_bf16 v[18:21], v[146:149], v[178:181], v[18:21]
	v_mfma_f32_16x16x32_bf16 v[10:13], v[154:157], v[178:181], v[10:13]
	v_mfma_f32_16x16x32_bf16 v[6:9], v[146:149], v[186:189], v[6:9]
	v_mfma_f32_16x16x32_bf16 v[2:5], v[154:157], v[186:189], v[2:5]
	v_mfma_f32_16x16x32_bf16 v[50:53], v[150:153], v[166:169], v[50:53]
	v_mfma_f32_16x16x32_bf16 v[42:45], v[158:161], v[166:169], v[42:45]
	v_mfma_f32_16x16x32_bf16 v[34:37], v[150:153], v[174:177], v[34:37]
	v_mfma_f32_16x16x32_bf16 v[26:29], v[158:161], v[174:177], v[26:29]
	v_mfma_f32_16x16x32_bf16 v[18:21], v[150:153], v[182:185], v[18:21]
	v_mfma_f32_16x16x32_bf16 v[10:13], v[158:161], v[182:185], v[10:13]
	v_mfma_f32_16x16x32_bf16 v[6:9], v[150:153], v[212:215], v[6:9]
	v_mfma_f32_16x16x32_bf16 v[2:5], v[158:161], v[212:215], v[2:5]
	s_barrier
	s_add_i32 s84, s84, 2
	s_addk_i32 s64, 0x100
	s_addk_i32 s65, 0x100
	s_cmp_gt_u32 s84, 29
	s_cbranch_scc0 .LBB0_114
	s_and_b64 vcc, exec, s[56:57]
	s_cbranch_vccz .LBB0_127
	s_barrier
	s_cmp_gt_i32 s61, 23
	s_mov_b64 s[46:47], -1
	s_cbranch_scc1 .LBB0_128

.LBB0_563:
	v_add_u32_e32 v3, 0x10000, v209
	ds_read_b128 v[140:143], v3
	ds_read_b128 v[144:147], v3 offset:1024
	ds_read_b128 v[148:151], v3 offset:2048
	ds_read_b128 v[152:155], v3 offset:3072
	v_add_u32_e32 v3, 0x14000, v209
	ds_read_b128 v[156:159], v3
	ds_read_b128 v[160:163], v3 offset:1024
	ds_read_b128 v[164:167], v3 offset:2048
	ds_read_b128 v[168:171], v3 offset:3072
	s_add_i32 s10, s57, 0xfff80080
	s_cmp_eq_u32 s59, 12
	s_cselect_b32 s62, s2, s10
	s_cselect_b32 s61, s3, s58
	s_add_i32 s60, s62, 0x80
	s_mov_b32 m0, s44
	ds_read_b128 v[172:175], v210
	ds_read_b128 v[176:179], v210 offset:1024
	ds_read_b128 v[180:183], v210 offset:2048
	ds_read_b128 v[184:187], v210 offset:3072
	ds_read_b128 v[188:191], v210 offset:4096
	ds_read_b128 v[192:195], v210 offset:5120
	ds_read_b128 v[196:199], v210 offset:6144
	ds_read_b128 v[200:203], v210 offset:7168
	buffer_load_dwordx4 v1, s[4:7], s57 offen lds
	s_mov_b32 m0, s45
	s_nop 0
	buffer_load_dwordx4 v206, s[4:7], s57 offen lds
	s_waitcnt vmcnt(8)
	s_waitcnt lgkmcnt(0)
	s_barrier
	s_waitcnt lgkmcnt(7)
	v_mfma_f32_16x16x32_bf16 v[130:133], v[140:143], v[172:175], v[130:133]
	v_mfma_f32_16x16x32_bf16 v[126:129], v[148:151], v[172:175], v[126:129]
	s_waitcnt lgkmcnt(5)
	v_mfma_f32_16x16x32_bf16 v[122:125], v[140:143], v[180:183], v[122:125]
	v_mfma_f32_16x16x32_bf16 v[118:121], v[148:151], v[180:183], v[118:121]
	s_waitcnt lgkmcnt(3)
	v_mfma_f32_16x16x32_bf16 v[114:117], v[140:143], v[188:191], v[114:117]
	v_mfma_f32_16x16x32_bf16 v[110:113], v[148:151], v[188:191], v[110:113]
	s_waitcnt lgkmcnt(1)
	v_mfma_f32_16x16x32_bf16 v[106:109], v[140:143], v[196:199], v[106:109]
	v_mfma_f32_16x16x32_bf16 v[102:105], v[148:151], v[196:199], v[102:105]
	v_mfma_f32_16x16x32_bf16 v[130:133], v[144:147], v[176:179], v[130:133]
	v_mfma_f32_16x16x32_bf16 v[126:129], v[152:155], v[176:179], v[126:129]
	v_mfma_f32_16x16x32_bf16 v[122:125], v[144:147], v[184:187], v[122:125]
	v_mfma_f32_16x16x32_bf16 v[118:121], v[152:155], v[184:187], v[118:121]
	v_mfma_f32_16x16x32_bf16 v[114:117], v[144:147], v[192:195], v[114:117]
	v_mfma_f32_16x16x32_bf16 v[110:113], v[152:155], v[192:195], v[110:113]
	s_waitcnt lgkmcnt(0)
	v_mfma_f32_16x16x32_bf16 v[106:109], v[144:147], v[200:203], v[106:109]
	v_mfma_f32_16x16x32_bf16 v[102:105], v[152:155], v[200:203], v[102:105]
	v_mfma_f32_16x16x32_bf16 v[98:101], v[156:159], v[172:175], v[98:101]
	v_mfma_f32_16x16x32_bf16 v[94:97], v[164:167], v[172:175], v[94:97]
	v_mfma_f32_16x16x32_bf16 v[90:93], v[156:159], v[180:183], v[90:93]
	v_mfma_f32_16x16x32_bf16 v[86:89], v[164:167], v[180:183], v[86:89]
	v_mfma_f32_16x16x32_bf16 v[82:85], v[156:159], v[188:191], v[82:85]
	v_mfma_f32_16x16x32_bf16 v[78:81], v[164:167], v[188:191], v[78:81]
	v_mfma_f32_16x16x32_bf16 v[74:77], v[156:159], v[196:199], v[74:77]
	v_mfma_f32_16x16x32_bf16 v[70:73], v[164:167], v[196:199], v[70:73]
	v_mfma_f32_16x16x32_bf16 v[98:101], v[160:163], v[176:179], v[98:101]
	v_mfma_f32_16x16x32_bf16 v[94:97], v[168:171], v[176:179], v[94:97]
	v_mfma_f32_16x16x32_bf16 v[90:93], v[160:163], v[184:187], v[90:93]
	v_mfma_f32_16x16x32_bf16 v[86:89], v[168:171], v[184:187], v[86:89]
	v_mfma_f32_16x16x32_bf16 v[82:85], v[160:163], v[192:195], v[82:85]
	v_mfma_f32_16x16x32_bf16 v[78:81], v[168:171], v[192:195], v[78:81]
	v_mfma_f32_16x16x32_bf16 v[74:77], v[160:163], v[200:203], v[74:77]
	v_mfma_f32_16x16x32_bf16 v[70:73], v[168:171], v[200:203], v[70:73]
	s_barrier
	s_mov_b32 m0, s28
	s_mov_b32 s10, s6
	s_mov_b32 s11, s7
	ds_read_b128 v[172:175], v210 offset:16384
	ds_read_b128 v[176:179], v210 offset:17408
	ds_read_b128 v[180:183], v210 offset:18432
	ds_read_b128 v[184:187], v210 offset:19456
	ds_read_b128 v[188:191], v210 offset:20480
	ds_read_b128 v[192:195], v210 offset:21504
	ds_read_b128 v[196:199], v210 offset:22528
	ds_read_b128 v[200:203], v210 offset:23552
	buffer_load_dwordx4 v135, s[8:11], s61 offen lds
	s_mov_b32 m0, s29
	s_add_i32 s63, s61, 0x80000
	buffer_load_dwordx4 v207, s[8:11], s61 offen lds
	s_mov_b32 m0, s30
	s_nop 0
	buffer_load_dwordx4 v135, s[8:11], s63 offen lds
	s_mov_b32 m0, s31
	s_nop 0
	buffer_load_dwordx4 v207, s[8:11], s63 offen lds
	s_mov_b32 m0, s27
	s_nop 0
	buffer_load_dwordx4 v1, s[4:7], s62 offen lds
	s_mov_b32 m0, s33
	s_nop 0
	buffer_load_dwordx4 v206, s[4:7], s62 offen lds
	s_waitcnt vmcnt(8)
	s_waitcnt lgkmcnt(0)
	s_barrier
	s_waitcnt lgkmcnt(7)
	v_mfma_f32_16x16x32_bf16 v[66:69], v[140:143], v[172:175], v[66:69]
	v_mfma_f32_16x16x32_bf16 v[62:65], v[148:151], v[172:175], v[62:65]
	s_waitcnt lgkmcnt(5)
	v_mfma_f32_16x16x32_bf16 v[58:61], v[140:143], v[180:183], v[58:61]
	v_mfma_f32_16x16x32_bf16 v[54:57], v[148:151], v[180:183], v[54:57]
	s_waitcnt lgkmcnt(3)
	v_mfma_f32_16x16x32_bf16 v[50:53], v[140:143], v[188:191], v[50:53]
	v_mfma_f32_16x16x32_bf16 v[46:49], v[148:151], v[188:191], v[46:49]
	s_waitcnt lgkmcnt(1)
	v_mfma_f32_16x16x32_bf16 v[42:45], v[140:143], v[196:199], v[42:45]
	v_mfma_f32_16x16x32_bf16 v[38:41], v[148:151], v[196:199], v[38:41]
	v_mfma_f32_16x16x32_bf16 v[66:69], v[144:147], v[176:179], v[66:69]
	v_mfma_f32_16x16x32_bf16 v[62:65], v[152:155], v[176:179], v[62:65]
	v_mfma_f32_16x16x32_bf16 v[58:61], v[144:147], v[184:187], v[58:61]
	v_mfma_f32_16x16x32_bf16 v[54:57], v[152:155], v[184:187], v[54:57]
	v_mfma_f32_16x16x32_bf16 v[50:53], v[144:147], v[192:195], v[50:53]
	v_mfma_f32_16x16x32_bf16 v[46:49], v[152:155], v[192:195], v[46:49]
	s_waitcnt lgkmcnt(0)
	v_mfma_f32_16x16x32_bf16 v[42:45], v[144:147], v[200:203], v[42:45]
	v_mfma_f32_16x16x32_bf16 v[38:41], v[152:155], v[200:203], v[38:41]
	v_mfma_f32_16x16x32_bf16 v[34:37], v[156:159], v[172:175], v[34:37]
	v_mfma_f32_16x16x32_bf16 v[30:33], v[164:167], v[172:175], v[30:33]
	v_mfma_f32_16x16x32_bf16 v[26:29], v[156:159], v[180:183], v[26:29]
	v_mfma_f32_16x16x32_bf16 v[22:25], v[164:167], v[180:183], v[22:25]
	v_mfma_f32_16x16x32_bf16 v[18:21], v[156:159], v[188:191], v[18:21]
	v_mfma_f32_16x16x32_bf16 v[14:17], v[164:167], v[188:191], v[14:17]
	v_mfma_f32_16x16x32_bf16 v[10:13], v[156:159], v[196:199], v[10:13]
	v_mfma_f32_16x16x32_bf16 v[4:7], v[164:167], v[196:199], v[6:9]
	v_mfma_f32_16x16x32_bf16 v[34:37], v[160:163], v[176:179], v[34:37]
	v_mfma_f32_16x16x32_bf16 v[30:33], v[168:171], v[176:179], v[30:33]
	v_mfma_f32_16x16x32_bf16 v[26:29], v[160:163], v[184:187], v[26:29]
	v_mfma_f32_16x16x32_bf16 v[22:25], v[168:171], v[184:187], v[22:25]
	v_mfma_f32_16x16x32_bf16 v[18:21], v[160:163], v[192:195], v[18:21]
	v_mfma_f32_16x16x32_bf16 v[14:17], v[168:171], v[192:195], v[14:17]
	v_mfma_f32_16x16x32_bf16 v[10:13], v[160:163], v[200:203], v[10:13]
	v_mfma_f32_16x16x32_bf16 v[4:7], v[168:171], v[200:203], v[4:7]
	s_barrier
	v_add_u32_e32 v3, 0x18000, v209
	ds_read_b128 v[140:143], v3
	ds_read_b128 v[144:147], v3 offset:1024
	ds_read_b128 v[148:151], v3 offset:2048
	ds_read_b128 v[152:155], v3 offset:3072
	v_add_u32_e32 v3, 0x1c000, v209
	ds_read_b128 v[156:159], v3
	ds_read_b128 v[160:163], v3 offset:1024
	ds_read_b128 v[164:167], v3 offset:2048
	ds_read_b128 v[168:171], v3 offset:3072
	s_add_i32 s62, s62, 0x80000
	s_mov_b32 m0, s34
	ds_read_b128 v[172:175], v210 offset:32768
	ds_read_b128 v[176:179], v210 offset:33792
	ds_read_b128 v[180:183], v210 offset:34816
	ds_read_b128 v[184:187], v210 offset:35840
	ds_read_b128 v[188:191], v210 offset:36864
	ds_read_b128 v[192:195], v210 offset:37888
	ds_read_b128 v[196:199], v210 offset:38912
	ds_read_b128 v[200:203], v210 offset:39936
	buffer_load_dwordx4 v1, s[4:7], s62 offen lds
	s_mov_b32 m0, s35
	s_nop 0
	buffer_load_dwordx4 v206, s[4:7], s62 offen lds
	s_waitcnt vmcnt(8)
	s_waitcnt lgkmcnt(0)
	s_barrier
	s_waitcnt lgkmcnt(7)
	v_mfma_f32_16x16x32_bf16 v[130:133], v[140:143], v[172:175], v[130:133]
	v_mfma_f32_16x16x32_bf16 v[126:129], v[148:151], v[172:175], v[126:129]
	s_waitcnt lgkmcnt(5)
	v_mfma_f32_16x16x32_bf16 v[122:125], v[140:143], v[180:183], v[122:125]
	v_mfma_f32_16x16x32_bf16 v[118:121], v[148:151], v[180:183], v[118:121]
	s_waitcnt lgkmcnt(3)
	v_mfma_f32_16x16x32_bf16 v[114:117], v[140:143], v[188:191], v[114:117]
	v_mfma_f32_16x16x32_bf16 v[110:113], v[148:151], v[188:191], v[110:113]
	s_waitcnt lgkmcnt(1)
	v_mfma_f32_16x16x32_bf16 v[106:109], v[140:143], v[196:199], v[106:109]
	v_mfma_f32_16x16x32_bf16 v[102:105], v[148:151], v[196:199], v[102:105]
	v_mfma_f32_16x16x32_bf16 v[130:133], v[144:147], v[176:179], v[130:133]
	v_mfma_f32_16x16x32_bf16 v[126:129], v[152:155], v[176:179], v[126:129]
	v_mfma_f32_16x16x32_bf16 v[122:125], v[144:147], v[184:187], v[122:125]
	v_mfma_f32_16x16x32_bf16 v[118:121], v[152:155], v[184:187], v[118:121]
	v_mfma_f32_16x16x32_bf16 v[114:117], v[144:147], v[192:195], v[114:117]
	v_mfma_f32_16x16x32_bf16 v[110:113], v[152:155], v[192:195], v[110:113]
	s_waitcnt lgkmcnt(0)
	v_mfma_f32_16x16x32_bf16 v[106:109], v[144:147], v[200:203], v[106:109]
	v_mfma_f32_16x16x32_bf16 v[102:105], v[152:155], v[200:203], v[102:105]
	v_mfma_f32_16x16x32_bf16 v[98:101], v[156:159], v[172:175], v[98:101]
	v_mfma_f32_16x16x32_bf16 v[94:97], v[164:167], v[172:175], v[94:97]
	v_mfma_f32_16x16x32_bf16 v[90:93], v[156:159], v[180:183], v[90:93]
	v_mfma_f32_16x16x32_bf16 v[86:89], v[164:167], v[180:183], v[86:89]
	v_mfma_f32_16x16x32_bf16 v[82:85], v[156:159], v[188:191], v[82:85]
	v_mfma_f32_16x16x32_bf16 v[78:81], v[164:167], v[188:191], v[78:81]
	v_mfma_f32_16x16x32_bf16 v[74:77], v[156:159], v[196:199], v[74:77]
	v_mfma_f32_16x16x32_bf16 v[70:73], v[164:167], v[196:199], v[70:73]
	v_mfma_f32_16x16x32_bf16 v[98:101], v[160:163], v[176:179], v[98:101]
	v_mfma_f32_16x16x32_bf16 v[94:97], v[168:171], v[176:179], v[94:97]
	v_mfma_f32_16x16x32_bf16 v[90:93], v[160:163], v[184:187], v[90:93]
	v_mfma_f32_16x16x32_bf16 v[86:89], v[168:171], v[184:187], v[86:89]
	v_mfma_f32_16x16x32_bf16 v[82:85], v[160:163], v[192:195], v[82:85]
	v_mfma_f32_16x16x32_bf16 v[78:81], v[168:171], v[192:195], v[78:81]
	v_mfma_f32_16x16x32_bf16 v[74:77], v[160:163], v[200:203], v[74:77]
	v_mfma_f32_16x16x32_bf16 v[70:73], v[168:171], v[200:203], v[70:73]
	s_barrier
	s_mov_b32 m0, s38
	s_add_i32 s62, s61, 0x80
	ds_read_b128 v[172:175], v210 offset:49152
	ds_read_b128 v[176:179], v210 offset:50176
	ds_read_b128 v[180:183], v210 offset:51200
	ds_read_b128 v[184:187], v210 offset:52224
	ds_read_b128 v[188:191], v210 offset:53248
	ds_read_b128 v[192:195], v210 offset:54272
	ds_read_b128 v[196:199], v210 offset:55296
	ds_read_b128 v[200:203], v210 offset:56320
	buffer_load_dwordx4 v135, s[8:11], s62 offen lds
	s_mov_b32 m0, s39
	s_add_i32 s61, s61, 0x80080
	buffer_load_dwordx4 v207, s[8:11], s62 offen lds
	s_mov_b32 m0, s42
	s_nop 0
	buffer_load_dwordx4 v135, s[8:11], s61 offen lds
	s_mov_b32 m0, s43
	s_nop 0
	buffer_load_dwordx4 v207, s[8:11], s61 offen lds
	s_mov_b32 m0, s40
	s_nop 0
	buffer_load_dwordx4 v1, s[4:7], s60 offen lds
	s_mov_b32 m0, s41
	s_nop 0
	buffer_load_dwordx4 v206, s[4:7], s60 offen lds
	s_waitcnt vmcnt(8)
	s_waitcnt lgkmcnt(0)
	s_barrier
	s_waitcnt lgkmcnt(7)
	v_mfma_f32_16x16x32_bf16 v[66:69], v[140:143], v[172:175], v[66:69]
	v_mfma_f32_16x16x32_bf16 v[62:65], v[148:151], v[172:175], v[62:65]
	s_waitcnt lgkmcnt(5)
	v_mfma_f32_16x16x32_bf16 v[58:61], v[140:143], v[180:183], v[58:61]
	v_mfma_f32_16x16x32_bf16 v[54:57], v[148:151], v[180:183], v[54:57]
	s_waitcnt lgkmcnt(3)
	v_mfma_f32_16x16x32_bf16 v[50:53], v[140:143], v[188:191], v[50:53]
	v_mfma_f32_16x16x32_bf16 v[46:49], v[148:151], v[188:191], v[46:49]
	s_waitcnt lgkmcnt(1)
	v_mfma_f32_16x16x32_bf16 v[42:45], v[140:143], v[196:199], v[42:45]
	v_mfma_f32_16x16x32_bf16 v[38:41], v[148:151], v[196:199], v[38:41]
	v_mfma_f32_16x16x32_bf16 v[66:69], v[144:147], v[176:179], v[66:69]
	v_mfma_f32_16x16x32_bf16 v[62:65], v[152:155], v[176:179], v[62:65]
	v_mfma_f32_16x16x32_bf16 v[58:61], v[144:147], v[184:187], v[58:61]
	v_mfma_f32_16x16x32_bf16 v[54:57], v[152:155], v[184:187], v[54:57]
	v_mfma_f32_16x16x32_bf16 v[50:53], v[144:147], v[192:195], v[50:53]
	v_mfma_f32_16x16x32_bf16 v[46:49], v[152:155], v[192:195], v[46:49]
	s_waitcnt lgkmcnt(0)
	v_mfma_f32_16x16x32_bf16 v[42:45], v[144:147], v[200:203], v[42:45]
	v_mfma_f32_16x16x32_bf16 v[38:41], v[152:155], v[200:203], v[38:41]
	v_mfma_f32_16x16x32_bf16 v[34:37], v[156:159], v[172:175], v[34:37]
	v_mfma_f32_16x16x32_bf16 v[30:33], v[164:167], v[172:175], v[30:33]
	v_mfma_f32_16x16x32_bf16 v[26:29], v[156:159], v[180:183], v[26:29]
	v_mfma_f32_16x16x32_bf16 v[22:25], v[164:167], v[180:183], v[22:25]
	v_mfma_f32_16x16x32_bf16 v[18:21], v[156:159], v[188:191], v[18:21]
	v_mfma_f32_16x16x32_bf16 v[14:17], v[164:167], v[188:191], v[14:17]
	v_mfma_f32_16x16x32_bf16 v[8:11], v[156:159], v[196:199], v[10:13]
	v_mfma_f32_16x16x32_bf16 v[4:7], v[164:167], v[196:199], v[4:7]
	v_mfma_f32_16x16x32_bf16 v[34:37], v[160:163], v[176:179], v[34:37]
	v_mfma_f32_16x16x32_bf16 v[30:33], v[168:171], v[176:179], v[30:33]
	v_mfma_f32_16x16x32_bf16 v[26:29], v[160:163], v[184:187], v[26:29]
	v_mfma_f32_16x16x32_bf16 v[22:25], v[168:171], v[184:187], v[22:25]
	v_mfma_f32_16x16x32_bf16 v[18:21], v[160:163], v[192:195], v[18:21]
	v_mfma_f32_16x16x32_bf16 v[14:17], v[168:171], v[192:195], v[14:17]
	v_mfma_f32_16x16x32_bf16 v[10:13], v[160:163], v[200:203], v[8:11]
	v_mfma_f32_16x16x32_bf16 v[6:9], v[168:171], v[200:203], v[4:7]
	s_barrier
	s_add_i32 s59, s59, 2
	s_addk_i32 s57, 0x100
	s_addk_i32 s58, 0x100
	s_cmp_gt_u32 s59, 13
	s_cbranch_scc0 .LBB0_563
	s_and_b64 vcc, exec, s[20:21]
	s_cbranch_vccz .LBB0_566
	s_barrier
.LBB0_566:
	s_lshl_b32 s2, s22, 8
	v_lshl_add_u32 v4, s23, 8, v208
	s_ashr_i32 s3, s2, 31
	v_ashrrev_i32_e32 v5, 31, v4
	s_cmp_lg_u32 s56, 0
	v_lshlrev_b64 v[4:5], 11, v[4:5]
	s_cselect_b64 s[10:11], -1, 0
	s_cmp_eq_u32 s56, 0
	v_lshl_add_u64 v[4:5], v[4:5], 0, s[2:3]
	s_cselect_b64 s[2:3], -1, 0
	s_and_b64 s[2:3], s[2:3], exec
	v_readlane_b32 s56, v255, 1
	s_cselect_b32 s22, s46, 0x11b00000
	v_readlane_b32 s58, v255, 3
	v_readlane_b32 s59, v255, 4
	s_add_u32 s22, s58, s22
	v_or_b32_e32 v4, v4, v134
	s_addc_u32 s23, s59, 0
	v_lshl_add_u64 v[140:141], v[4:5], 1, s[22:23]
	v_add_co_u32_e32 v154, vcc, 0x10000, v140
	global_load_dwordx4 v[142:145], v[140:141], off nt
	global_load_dwordx4 v[146:149], v[140:141], off offset:256 nt
	v_addc_co_u32_e32 v155, vcc, 0, v141, vcc
	v_add_co_u32_e32 v162, vcc, 0x20000, v140
	global_load_dwordx4 v[150:153], v[154:155], off nt
	s_nop 0
	global_load_dwordx4 v[154:157], v[154:155], off offset:256 nt
	v_addc_co_u32_e32 v163, vcc, 0, v141, vcc
	global_load_dwordx4 v[158:161], v[162:163], off nt
	global_load_dwordx4 v[212:215], v[162:163], off offset:256 nt
	v_add_co_u32_e32 v162, vcc, 0x30000, v140
	s_mov_b64 s[22:23], -1
	s_nop 0
	v_addc_co_u32_e32 v163, vcc, 0, v141, vcc
	global_load_dwordx4 v[216:219], v[162:163], off nt
	global_load_dwordx4 v[220:223], v[162:163], off offset:256 nt
	v_lshl_add_u64 v[4:5], v[4:5], 1, s[18:19]
	s_mov_b64 vcc, s[2:3]
	v_readlane_b32 s57, v255, 2
	v_readlane_b32 s60, v255, 5
	v_readlane_b32 s61, v255, 6
	v_readlane_b32 s62, v255, 7
	v_readlane_b32 s63, v255, 8
	s_waitcnt vmcnt(7)
	v_cvt_f32_f16_sdwa v203, v142 dst_sel:DWORD dst_unused:UNUSED_PAD src0_sel:WORD_1
	v_cvt_f32_f16_e32 v202, v142
	v_cvt_f32_f16_sdwa v205, v143 dst_sel:DWORD dst_unused:UNUSED_PAD src0_sel:WORD_1
	v_cvt_f32_f16_e32 v204, v143
	v_cvt_f32_f16_sdwa v199, v144 dst_sel:DWORD dst_unused:UNUSED_PAD src0_sel:WORD_1
	v_cvt_f32_f16_e32 v198, v144
	v_cvt_f32_f16_sdwa v201, v145 dst_sel:DWORD dst_unused:UNUSED_PAD src0_sel:WORD_1
	v_cvt_f32_f16_e32 v200, v145
	s_waitcnt vmcnt(6)
	v_cvt_f32_f16_sdwa v195, v146 dst_sel:DWORD dst_unused:UNUSED_PAD src0_sel:WORD_1
	v_cvt_f32_f16_e32 v194, v146
	v_cvt_f32_f16_sdwa v197, v147 dst_sel:DWORD dst_unused:UNUSED_PAD src0_sel:WORD_1
	v_cvt_f32_f16_e32 v196, v147
	v_cvt_f32_f16_sdwa v191, v148 dst_sel:DWORD dst_unused:UNUSED_PAD src0_sel:WORD_1
	v_cvt_f32_f16_e32 v190, v148
	v_cvt_f32_f16_sdwa v193, v149 dst_sel:DWORD dst_unused:UNUSED_PAD src0_sel:WORD_1
	v_cvt_f32_f16_e32 v192, v149
	s_waitcnt vmcnt(5)
	v_cvt_f32_f16_sdwa v187, v150 dst_sel:DWORD dst_unused:UNUSED_PAD src0_sel:WORD_1
	v_cvt_f32_f16_e32 v186, v150
	v_cvt_f32_f16_sdwa v189, v151 dst_sel:DWORD dst_unused:UNUSED_PAD src0_sel:WORD_1
	v_cvt_f32_f16_e32 v188, v151
	v_cvt_f32_f16_sdwa v183, v152 dst_sel:DWORD dst_unused:UNUSED_PAD src0_sel:WORD_1
	v_cvt_f32_f16_e32 v182, v152
	v_cvt_f32_f16_sdwa v185, v153 dst_sel:DWORD dst_unused:UNUSED_PAD src0_sel:WORD_1
	v_cvt_f32_f16_e32 v184, v153
	s_waitcnt vmcnt(4)
	v_cvt_f32_f16_sdwa v179, v154 dst_sel:DWORD dst_unused:UNUSED_PAD src0_sel:WORD_1
	v_cvt_f32_f16_e32 v178, v154
	v_cvt_f32_f16_sdwa v181, v155 dst_sel:DWORD dst_unused:UNUSED_PAD src0_sel:WORD_1
	v_cvt_f32_f16_e32 v180, v155
	v_cvt_f32_f16_sdwa v175, v156 dst_sel:DWORD dst_unused:UNUSED_PAD src0_sel:WORD_1
	v_cvt_f32_f16_e32 v174, v156
	v_cvt_f32_f16_sdwa v177, v157 dst_sel:DWORD dst_unused:UNUSED_PAD src0_sel:WORD_1
	v_cvt_f32_f16_e32 v176, v157
	s_waitcnt vmcnt(3)
	v_cvt_f32_f16_sdwa v171, v158 dst_sel:DWORD dst_unused:UNUSED_PAD src0_sel:WORD_1
	v_cvt_f32_f16_e32 v170, v158
	v_cvt_f32_f16_sdwa v173, v159 dst_sel:DWORD dst_unused:UNUSED_PAD src0_sel:WORD_1
	v_cvt_f32_f16_e32 v172, v159
	v_cvt_f32_f16_sdwa v167, v160 dst_sel:DWORD dst_unused:UNUSED_PAD src0_sel:WORD_1
	v_cvt_f32_f16_e32 v166, v160
	v_cvt_f32_f16_sdwa v169, v161 dst_sel:DWORD dst_unused:UNUSED_PAD src0_sel:WORD_1
	v_cvt_f32_f16_e32 v168, v161
	s_waitcnt vmcnt(2)
	v_cvt_f32_f16_sdwa v163, v212 dst_sel:DWORD dst_unused:UNUSED_PAD src0_sel:WORD_1
	v_cvt_f32_f16_e32 v162, v212
	v_cvt_f32_f16_sdwa v165, v213 dst_sel:DWORD dst_unused:UNUSED_PAD src0_sel:WORD_1
	v_cvt_f32_f16_e32 v164, v213
	v_cvt_f32_f16_sdwa v159, v214 dst_sel:DWORD dst_unused:UNUSED_PAD src0_sel:WORD_1
	v_cvt_f32_f16_e32 v158, v214
	v_cvt_f32_f16_sdwa v161, v215 dst_sel:DWORD dst_unused:UNUSED_PAD src0_sel:WORD_1
	v_cvt_f32_f16_e32 v160, v215
	s_waitcnt vmcnt(1)
	v_cvt_f32_f16_sdwa v155, v216 dst_sel:DWORD dst_unused:UNUSED_PAD src0_sel:WORD_1
	v_cvt_f32_f16_e32 v154, v216
	v_cvt_f32_f16_sdwa v157, v217 dst_sel:DWORD dst_unused:UNUSED_PAD src0_sel:WORD_1
	v_cvt_f32_f16_e32 v156, v217
	v_cvt_f32_f16_sdwa v151, v218 dst_sel:DWORD dst_unused:UNUSED_PAD src0_sel:WORD_1
	v_cvt_f32_f16_e32 v150, v218
	v_cvt_f32_f16_sdwa v153, v219 dst_sel:DWORD dst_unused:UNUSED_PAD src0_sel:WORD_1
	v_cvt_f32_f16_e32 v152, v219
	s_waitcnt vmcnt(0)
	v_cvt_f32_f16_sdwa v147, v220 dst_sel:DWORD dst_unused:UNUSED_PAD src0_sel:WORD_1
	v_cvt_f32_f16_e32 v146, v220
	v_cvt_f32_f16_sdwa v149, v221 dst_sel:DWORD dst_unused:UNUSED_PAD src0_sel:WORD_1
	v_cvt_f32_f16_e32 v148, v221
	v_cvt_f32_f16_sdwa v143, v222 dst_sel:DWORD dst_unused:UNUSED_PAD src0_sel:WORD_1
	v_cvt_f32_f16_e32 v142, v222
	v_cvt_f32_f16_sdwa v145, v223 dst_sel:DWORD dst_unused:UNUSED_PAD src0_sel:WORD_1
	v_cvt_f32_f16_e32 v144, v223
	s_cbranch_vccnz .LBB0_568
	v_pk_mul_f32 v[212:213], v[130:131], v[202:203]
	v_pk_mul_f32 v[214:215], v[132:133], v[204:205]
	v_pk_mul_f32 v[216:217], v[126:127], v[198:199]
	v_pk_mul_f32 v[218:219], v[128:129], v[200:201]
	v_cvt_pk_bf16_f32 v212, v212, v213
	v_cvt_pk_bf16_f32 v213, v214, v215
	v_cvt_pk_bf16_f32 v214, v216, v217
	v_cvt_pk_bf16_f32 v215, v218, v219
	global_store_dwordx4 v[4:5], v[212:215], off
	v_pk_mul_f32 v[216:217], v[94:95], v[190:191]
	v_pk_mul_f32 v[218:219], v[96:97], v[192:193]
	v_pk_mul_f32 v[212:213], v[98:99], v[194:195]
	v_pk_mul_f32 v[214:215], v[100:101], v[196:197]
	v_cvt_pk_bf16_f32 v212, v212, v213
	v_cvt_pk_bf16_f32 v213, v214, v215
	v_cvt_pk_bf16_f32 v214, v216, v217
	v_cvt_pk_bf16_f32 v215, v218, v219
	global_store_dwordx4 v[4:5], v[212:215], off offset:256
	v_pk_mul_f32 v[216:217], v[118:119], v[182:183]
	v_pk_mul_f32 v[218:219], v[120:121], v[184:185]
	v_pk_mul_f32 v[212:213], v[122:123], v[186:187]
	v_pk_mul_f32 v[214:215], v[124:125], v[188:189]
	v_cvt_pk_bf16_f32 v212, v212, v213
	v_cvt_pk_bf16_f32 v213, v214, v215
	v_cvt_pk_bf16_f32 v214, v216, v217
	v_add_co_u32_e32 v216, vcc, s36, v4
	v_cvt_pk_bf16_f32 v215, v218, v219
	s_nop 0
	v_addc_co_u32_e32 v217, vcc, 0, v5, vcc
	global_store_dwordx4 v[216:217], v[212:215], off
	v_pk_mul_f32 v[218:219], v[86:87], v[174:175]
	v_pk_mul_f32 v[220:221], v[88:89], v[176:177]
	v_pk_mul_f32 v[212:213], v[90:91], v[178:179]
	v_pk_mul_f32 v[214:215], v[92:93], v[180:181]
	v_cvt_pk_bf16_f32 v212, v212, v213
	v_cvt_pk_bf16_f32 v213, v214, v215
	v_cvt_pk_bf16_f32 v214, v218, v219
	v_cvt_pk_bf16_f32 v215, v220, v221
	global_store_dwordx4 v[216:217], v[212:215], off offset:256
	v_pk_mul_f32 v[216:217], v[110:111], v[166:167]
	v_pk_mul_f32 v[218:219], v[112:113], v[168:169]
	v_pk_mul_f32 v[212:213], v[114:115], v[170:171]
	v_pk_mul_f32 v[214:215], v[116:117], v[172:173]
	v_cvt_pk_bf16_f32 v212, v212, v213
	v_cvt_pk_bf16_f32 v213, v214, v215
	v_cvt_pk_bf16_f32 v214, v216, v217
	v_add_co_u32_e32 v216, vcc, s7, v4
	v_cvt_pk_bf16_f32 v215, v218, v219
	s_nop 0
	v_addc_co_u32_e32 v217, vcc, 0, v5, vcc
	global_store_dwordx4 v[216:217], v[212:215], off
	v_pk_mul_f32 v[218:219], v[78:79], v[158:159]
	v_pk_mul_f32 v[220:221], v[80:81], v[160:161]
	v_pk_mul_f32 v[212:213], v[82:83], v[162:163]
	v_pk_mul_f32 v[214:215], v[84:85], v[164:165]
	v_cvt_pk_bf16_f32 v212, v212, v213
	v_cvt_pk_bf16_f32 v213, v214, v215
	v_cvt_pk_bf16_f32 v214, v218, v219
	v_cvt_pk_bf16_f32 v215, v220, v221
	global_store_dwordx4 v[216:217], v[212:215], off offset:256
	v_pk_mul_f32 v[216:217], v[102:103], v[150:151]
	v_pk_mul_f32 v[218:219], v[104:105], v[152:153]
	v_pk_mul_f32 v[212:213], v[106:107], v[154:155]
	v_pk_mul_f32 v[214:215], v[108:109], v[156:157]
	v_cvt_pk_bf16_f32 v212, v212, v213
	v_cvt_pk_bf16_f32 v213, v214, v215
	v_cvt_pk_bf16_f32 v214, v216, v217
	v_add_co_u32_e32 v216, vcc, s47, v4
	v_cvt_pk_bf16_f32 v215, v218, v219
	s_nop 0
	v_addc_co_u32_e32 v217, vcc, 0, v5, vcc
	global_store_dwordx4 v[216:217], v[212:215], off
	v_pk_mul_f32 v[218:219], v[70:71], v[142:143]
	v_pk_mul_f32 v[220:221], v[72:73], v[144:145]
	v_pk_mul_f32 v[212:213], v[74:75], v[146:147]
	v_pk_mul_f32 v[214:215], v[76:77], v[148:149]
	v_cvt_pk_bf16_f32 v212, v212, v213
	v_cvt_pk_bf16_f32 v213, v214, v215
	v_cvt_pk_bf16_f32 v214, v218, v219
	v_cvt_pk_bf16_f32 v215, v220, v221
	s_mov_b64 s[22:23], 0
	global_store_dwordx4 v[216:217], v[212:215], off offset:256

.LBB0_570:
	v_add_co_u32_e32 v146, vcc, s37, v140
	v_cndmask_b32_e64 v3, 0, 1, s[10:11]
	s_nop 0
	v_addc_co_u32_e32 v147, vcc, 0, v141, vcc
	v_add_co_u32_e32 v154, vcc, s48, v140
	global_load_dwordx4 v[142:145], v[146:147], off nt
	s_nop 0
	global_load_dwordx4 v[146:149], v[146:147], off offset:256 nt
	v_addc_co_u32_e32 v155, vcc, 0, v141, vcc
	v_add_co_u32_e32 v162, vcc, 0xa0000, v140
	global_load_dwordx4 v[150:153], v[154:155], off nt
	s_nop 0
	global_load_dwordx4 v[154:157], v[154:155], off offset:256 nt
	v_addc_co_u32_e32 v163, vcc, 0, v141, vcc
	v_add_co_u32_e32 v140, vcc, 0xb0000, v140
	global_load_dwordx4 v[158:161], v[162:163], off nt
	global_load_dwordx4 v[212:215], v[162:163], off offset:256 nt
	v_addc_co_u32_e32 v141, vcc, 0, v141, vcc
	global_load_dwordx4 v[216:219], v[140:141], off nt
	global_load_dwordx4 v[220:223], v[140:141], off offset:256 nt
	v_cmp_ne_u32_e64 s[2:3], 1, v3
	s_andn2_b64 vcc, exec, s[10:11]
	s_mov_b64 s[10:11], -1
	s_waitcnt vmcnt(7)
	v_cvt_f32_f16_sdwa v201, v142 dst_sel:DWORD dst_unused:UNUSED_PAD src0_sel:WORD_1
	v_cvt_f32_f16_e32 v200, v142
	v_cvt_f32_f16_sdwa v203, v143 dst_sel:DWORD dst_unused:UNUSED_PAD src0_sel:WORD_1
	v_cvt_f32_f16_e32 v202, v143
	v_cvt_f32_f16_sdwa v197, v144 dst_sel:DWORD dst_unused:UNUSED_PAD src0_sel:WORD_1
	v_cvt_f32_f16_e32 v196, v144
	v_cvt_f32_f16_sdwa v199, v145 dst_sel:DWORD dst_unused:UNUSED_PAD src0_sel:WORD_1
	v_cvt_f32_f16_e32 v198, v145
	s_waitcnt vmcnt(6)
	v_cvt_f32_f16_sdwa v193, v146 dst_sel:DWORD dst_unused:UNUSED_PAD src0_sel:WORD_1
	v_cvt_f32_f16_e32 v192, v146
	v_cvt_f32_f16_sdwa v195, v147 dst_sel:DWORD dst_unused:UNUSED_PAD src0_sel:WORD_1
	v_cvt_f32_f16_e32 v194, v147
	v_cvt_f32_f16_sdwa v189, v148 dst_sel:DWORD dst_unused:UNUSED_PAD src0_sel:WORD_1
	v_cvt_f32_f16_e32 v188, v148
	v_cvt_f32_f16_sdwa v191, v149 dst_sel:DWORD dst_unused:UNUSED_PAD src0_sel:WORD_1
	v_cvt_f32_f16_e32 v190, v149
	s_waitcnt vmcnt(5)
	v_cvt_f32_f16_sdwa v185, v150 dst_sel:DWORD dst_unused:UNUSED_PAD src0_sel:WORD_1
	v_cvt_f32_f16_e32 v184, v150
	v_cvt_f32_f16_sdwa v187, v151 dst_sel:DWORD dst_unused:UNUSED_PAD src0_sel:WORD_1
	v_cvt_f32_f16_e32 v186, v151
	v_cvt_f32_f16_sdwa v181, v152 dst_sel:DWORD dst_unused:UNUSED_PAD src0_sel:WORD_1
	v_cvt_f32_f16_e32 v180, v152
	v_cvt_f32_f16_sdwa v183, v153 dst_sel:DWORD dst_unused:UNUSED_PAD src0_sel:WORD_1
	v_cvt_f32_f16_e32 v182, v153
	s_waitcnt vmcnt(4)
	v_cvt_f32_f16_sdwa v177, v154 dst_sel:DWORD dst_unused:UNUSED_PAD src0_sel:WORD_1
	v_cvt_f32_f16_e32 v176, v154
	v_cvt_f32_f16_sdwa v179, v155 dst_sel:DWORD dst_unused:UNUSED_PAD src0_sel:WORD_1
	v_cvt_f32_f16_e32 v178, v155
	v_cvt_f32_f16_sdwa v173, v156 dst_sel:DWORD dst_unused:UNUSED_PAD src0_sel:WORD_1
	v_cvt_f32_f16_e32 v172, v156
	v_cvt_f32_f16_sdwa v175, v157 dst_sel:DWORD dst_unused:UNUSED_PAD src0_sel:WORD_1
	v_cvt_f32_f16_e32 v174, v157
	s_waitcnt vmcnt(3)
	v_cvt_f32_f16_sdwa v169, v158 dst_sel:DWORD dst_unused:UNUSED_PAD src0_sel:WORD_1
	v_cvt_f32_f16_e32 v168, v158
	v_cvt_f32_f16_sdwa v171, v159 dst_sel:DWORD dst_unused:UNUSED_PAD src0_sel:WORD_1
	v_cvt_f32_f16_e32 v170, v159
	v_cvt_f32_f16_sdwa v165, v160 dst_sel:DWORD dst_unused:UNUSED_PAD src0_sel:WORD_1
	v_cvt_f32_f16_e32 v164, v160
	v_cvt_f32_f16_sdwa v167, v161 dst_sel:DWORD dst_unused:UNUSED_PAD src0_sel:WORD_1
	v_cvt_f32_f16_e32 v166, v161
	s_waitcnt vmcnt(2)
	v_cvt_f32_f16_sdwa v161, v212 dst_sel:DWORD dst_unused:UNUSED_PAD src0_sel:WORD_1
	v_cvt_f32_f16_e32 v160, v212
	v_cvt_f32_f16_sdwa v163, v213 dst_sel:DWORD dst_unused:UNUSED_PAD src0_sel:WORD_1
	v_cvt_f32_f16_e32 v162, v213
	v_cvt_f32_f16_sdwa v157, v214 dst_sel:DWORD dst_unused:UNUSED_PAD src0_sel:WORD_1
	v_cvt_f32_f16_e32 v156, v214
	v_cvt_f32_f16_sdwa v159, v215 dst_sel:DWORD dst_unused:UNUSED_PAD src0_sel:WORD_1
	v_cvt_f32_f16_e32 v158, v215
	s_waitcnt vmcnt(1)
	v_cvt_f32_f16_sdwa v153, v216 dst_sel:DWORD dst_unused:UNUSED_PAD src0_sel:WORD_1
	v_cvt_f32_f16_e32 v152, v216
	v_cvt_f32_f16_sdwa v155, v217 dst_sel:DWORD dst_unused:UNUSED_PAD src0_sel:WORD_1
	v_cvt_f32_f16_e32 v154, v217
	v_cvt_f32_f16_sdwa v149, v218 dst_sel:DWORD dst_unused:UNUSED_PAD src0_sel:WORD_1
	v_cvt_f32_f16_e32 v148, v218
	v_cvt_f32_f16_sdwa v151, v219 dst_sel:DWORD dst_unused:UNUSED_PAD src0_sel:WORD_1
	v_cvt_f32_f16_e32 v150, v219
	s_waitcnt vmcnt(0)
	v_cvt_f32_f16_sdwa v145, v220 dst_sel:DWORD dst_unused:UNUSED_PAD src0_sel:WORD_1
	v_cvt_f32_f16_e32 v144, v220
	v_cvt_f32_f16_sdwa v147, v221 dst_sel:DWORD dst_unused:UNUSED_PAD src0_sel:WORD_1
	v_cvt_f32_f16_e32 v146, v221
	v_cvt_f32_f16_sdwa v141, v222 dst_sel:DWORD dst_unused:UNUSED_PAD src0_sel:WORD_1
	v_cvt_f32_f16_e32 v140, v222
	v_cvt_f32_f16_sdwa v143, v223 dst_sel:DWORD dst_unused:UNUSED_PAD src0_sel:WORD_1
	v_cvt_f32_f16_e32 v142, v223
	s_cbranch_vccnz .LBB0_572
	v_pk_mul_f32 v[204:205], v[66:67], v[200:201]
	v_pk_mul_f32 v[214:215], v[68:69], v[202:203]
	v_pk_mul_f32 v[216:217], v[62:63], v[196:197]
	v_pk_mul_f32 v[218:219], v[64:65], v[198:199]
	v_cvt_pk_bf16_f32 v212, v204, v205
	v_add_co_u32_e32 v204, vcc, s37, v4
	v_cvt_pk_bf16_f32 v213, v214, v215
	v_cvt_pk_bf16_f32 v214, v216, v217
	v_cvt_pk_bf16_f32 v215, v218, v219
	v_addc_co_u32_e32 v205, vcc, 0, v5, vcc
	global_store_dwordx4 v[204:205], v[212:215], off
	v_pk_mul_f32 v[216:217], v[30:31], v[188:189]
	v_pk_mul_f32 v[218:219], v[32:33], v[190:191]
	v_pk_mul_f32 v[212:213], v[34:35], v[192:193]
	v_pk_mul_f32 v[214:215], v[36:37], v[194:195]
	v_cvt_pk_bf16_f32 v212, v212, v213
	v_cvt_pk_bf16_f32 v213, v214, v215
	v_cvt_pk_bf16_f32 v214, v216, v217
	v_cvt_pk_bf16_f32 v215, v218, v219
	global_store_dwordx4 v[204:205], v[212:215], off offset:256
	v_pk_mul_f32 v[204:205], v[58:59], v[184:185]
	v_pk_mul_f32 v[216:217], v[54:55], v[180:181]
	v_pk_mul_f32 v[214:215], v[60:61], v[186:187]
	v_pk_mul_f32 v[218:219], v[56:57], v[182:183]
	v_cvt_pk_bf16_f32 v212, v204, v205
	v_add_co_u32_e32 v204, vcc, s48, v4
	v_cvt_pk_bf16_f32 v213, v214, v215
	v_cvt_pk_bf16_f32 v214, v216, v217
	v_cvt_pk_bf16_f32 v215, v218, v219
	v_addc_co_u32_e32 v205, vcc, 0, v5, vcc
	global_store_dwordx4 v[204:205], v[212:215], off
	v_pk_mul_f32 v[216:217], v[22:23], v[172:173]
	v_pk_mul_f32 v[218:219], v[24:25], v[174:175]
	v_pk_mul_f32 v[212:213], v[26:27], v[176:177]
	v_pk_mul_f32 v[214:215], v[28:29], v[178:179]
	v_cvt_pk_bf16_f32 v212, v212, v213
	v_cvt_pk_bf16_f32 v213, v214, v215
	v_cvt_pk_bf16_f32 v214, v216, v217
	v_cvt_pk_bf16_f32 v215, v218, v219
	global_store_dwordx4 v[204:205], v[212:215], off offset:256
	v_pk_mul_f32 v[204:205], v[50:51], v[168:169]
	v_pk_mul_f32 v[216:217], v[46:47], v[164:165]
	v_pk_mul_f32 v[214:215], v[52:53], v[170:171]
	v_pk_mul_f32 v[218:219], v[48:49], v[166:167]
	v_cvt_pk_bf16_f32 v212, v204, v205
	v_add_co_u32_e32 v204, vcc, s49, v4
	v_cvt_pk_bf16_f32 v213, v214, v215
	v_cvt_pk_bf16_f32 v214, v216, v217
	v_cvt_pk_bf16_f32 v215, v218, v219
	v_addc_co_u32_e32 v205, vcc, 0, v5, vcc
	global_store_dwordx4 v[204:205], v[212:215], off
	v_pk_mul_f32 v[216:217], v[14:15], v[156:157]
	v_pk_mul_f32 v[218:219], v[16:17], v[158:159]
	v_pk_mul_f32 v[212:213], v[18:19], v[160:161]
	v_pk_mul_f32 v[214:215], v[20:21], v[162:163]
	v_cvt_pk_bf16_f32 v212, v212, v213
	v_cvt_pk_bf16_f32 v213, v214, v215
	v_cvt_pk_bf16_f32 v214, v216, v217
	v_cvt_pk_bf16_f32 v215, v218, v219
	global_store_dwordx4 v[204:205], v[212:215], off offset:256
	v_pk_mul_f32 v[204:205], v[42:43], v[152:153]
	v_pk_mul_f32 v[216:217], v[38:39], v[148:149]
	v_pk_mul_f32 v[214:215], v[44:45], v[154:155]
	v_pk_mul_f32 v[218:219], v[40:41], v[150:151]
	v_add_co_u32_e32 v4, vcc, s50, v4
	v_cvt_pk_bf16_f32 v212, v204, v205
	v_cvt_pk_bf16_f32 v213, v214, v215
	v_cvt_pk_bf16_f32 v214, v216, v217
	v_cvt_pk_bf16_f32 v215, v218, v219
	v_addc_co_u32_e32 v5, vcc, 0, v5, vcc
	global_store_dwordx4 v[4:5], v[212:215], off
	v_pk_mul_f32 v[204:205], v[10:11], v[144:145]
	v_pk_mul_f32 v[216:217], v[6:7], v[140:141]
	v_pk_mul_f32 v[214:215], v[12:13], v[146:147]
	v_pk_mul_f32 v[218:219], v[8:9], v[142:143]
	v_cvt_pk_bf16_f32 v212, v204, v205
	v_cvt_pk_bf16_f32 v213, v214, v215
	v_cvt_pk_bf16_f32 v214, v216, v217
	v_cvt_pk_bf16_f32 v215, v218, v219
	s_mov_b64 s[10:11], 0
	global_store_dwordx4 v[4:5], v[212:215], off offset:256

.LBB0_686:
	v_add_u32_e32 v152, 0x10000, v138
	v_add_u32_e32 v168, 0x14000, v138
	ds_read_b128 v[140:143], v152
	ds_read_b128 v[144:147], v152 offset:1024
	ds_read_b128 v[148:151], v152 offset:2048
	ds_read_b128 v[152:155], v152 offset:3072
	ds_read_b128 v[156:159], v168
	ds_read_b128 v[160:163], v168 offset:1024
	ds_read_b128 v[164:167], v168 offset:2048
	ds_read_b128 v[168:171], v168 offset:3072
	s_add_i32 s10, s33, s52
	s_add_i32 s53, s27, s52
	s_add_i32 s11, s10, 0x1000
	s_addk_i32 s53, 0x1000
	s_cmp_eq_u32 s52, 0
	s_cselect_b32 s55, s49, s11
	s_cselect_b32 s54, s50, s53
	s_or_b32 s53, s55, 0x80
	s_add_i32 s10, s10, 0x80f80
	s_mov_b32 m0, s43
	ds_read_b128 v[172:175], v139
	ds_read_b128 v[176:179], v139 offset:1024
	ds_read_b128 v[180:183], v139 offset:2048
	ds_read_b128 v[184:187], v139 offset:3072
	ds_read_b128 v[188:191], v139 offset:4096
	ds_read_b128 v[192:195], v139 offset:5120
	ds_read_b128 v[196:199], v139 offset:6144
	ds_read_b128 v[200:203], v139 offset:7168
	buffer_load_dwordx4 v134, s[4:7], s10 offen lds
	s_mov_b32 m0, s44
	s_nop 0
	buffer_load_dwordx4 v136, s[4:7], s10 offen lds
	s_waitcnt vmcnt(8)
	s_waitcnt lgkmcnt(0)
	s_barrier
	s_waitcnt lgkmcnt(7)
	v_mfma_f32_16x16x32_bf16 v[126:129], v[140:143], v[172:175], v[126:129]
	v_mfma_f32_16x16x32_bf16 v[122:125], v[148:151], v[172:175], v[122:125]
	s_waitcnt lgkmcnt(5)
	v_mfma_f32_16x16x32_bf16 v[110:113], v[140:143], v[180:183], v[110:113]
	v_mfma_f32_16x16x32_bf16 v[106:109], v[148:151], v[180:183], v[106:109]
	s_waitcnt lgkmcnt(3)
	v_mfma_f32_16x16x32_bf16 v[98:101], v[140:143], v[188:191], v[98:101]
	v_mfma_f32_16x16x32_bf16 v[90:93], v[148:151], v[188:191], v[90:93]
	s_waitcnt lgkmcnt(1)
	v_mfma_f32_16x16x32_bf16 v[82:85], v[140:143], v[196:199], v[82:85]
	v_mfma_f32_16x16x32_bf16 v[74:77], v[148:151], v[196:199], v[74:77]
	v_mfma_f32_16x16x32_bf16 v[126:129], v[144:147], v[176:179], v[126:129]
	v_mfma_f32_16x16x32_bf16 v[122:125], v[152:155], v[176:179], v[122:125]
	v_mfma_f32_16x16x32_bf16 v[110:113], v[144:147], v[184:187], v[110:113]
	v_mfma_f32_16x16x32_bf16 v[106:109], v[152:155], v[184:187], v[106:109]
	v_mfma_f32_16x16x32_bf16 v[98:101], v[144:147], v[192:195], v[98:101]
	v_mfma_f32_16x16x32_bf16 v[90:93], v[152:155], v[192:195], v[90:93]
	s_waitcnt lgkmcnt(0)
	v_mfma_f32_16x16x32_bf16 v[82:85], v[144:147], v[200:203], v[82:85]
	v_mfma_f32_16x16x32_bf16 v[74:77], v[152:155], v[200:203], v[74:77]
	v_mfma_f32_16x16x32_bf16 v[118:121], v[156:159], v[172:175], v[118:121]
	v_mfma_f32_16x16x32_bf16 v[114:117], v[164:167], v[172:175], v[114:117]
	v_mfma_f32_16x16x32_bf16 v[102:105], v[156:159], v[180:183], v[102:105]
	v_mfma_f32_16x16x32_bf16 v[94:97], v[164:167], v[180:183], v[94:97]
	v_mfma_f32_16x16x32_bf16 v[86:89], v[156:159], v[188:191], v[86:89]
	v_mfma_f32_16x16x32_bf16 v[78:81], v[164:167], v[188:191], v[78:81]
	v_mfma_f32_16x16x32_bf16 v[70:73], v[156:159], v[196:199], v[70:73]
	v_mfma_f32_16x16x32_bf16 v[66:69], v[164:167], v[196:199], v[66:69]
	v_mfma_f32_16x16x32_bf16 v[118:121], v[160:163], v[176:179], v[118:121]
	v_mfma_f32_16x16x32_bf16 v[114:117], v[168:171], v[176:179], v[114:117]
	v_mfma_f32_16x16x32_bf16 v[102:105], v[160:163], v[184:187], v[102:105]
	v_mfma_f32_16x16x32_bf16 v[94:97], v[168:171], v[184:187], v[94:97]
	v_mfma_f32_16x16x32_bf16 v[86:89], v[160:163], v[192:195], v[86:89]
	v_mfma_f32_16x16x32_bf16 v[78:81], v[168:171], v[192:195], v[78:81]
	v_mfma_f32_16x16x32_bf16 v[70:73], v[160:163], v[200:203], v[70:73]
	v_mfma_f32_16x16x32_bf16 v[66:69], v[168:171], v[200:203], v[66:69]
	s_barrier
	s_mov_b32 m0, s26
	s_mov_b32 s10, s6
	s_mov_b32 s11, s7
	ds_read_b128 v[172:175], v139 offset:16384
	ds_read_b128 v[176:179], v139 offset:17408
	ds_read_b128 v[180:183], v139 offset:18432
	ds_read_b128 v[184:187], v139 offset:19456
	ds_read_b128 v[188:191], v139 offset:20480
	ds_read_b128 v[192:195], v139 offset:21504
	ds_read_b128 v[196:199], v139 offset:22528
	ds_read_b128 v[200:203], v139 offset:23552
	buffer_load_dwordx4 v135, s[8:11], s54 offen lds
	s_mov_b32 m0, s28
	s_add_i32 s56, s54, 0x80000
	buffer_load_dwordx4 v137, s[8:11], s54 offen lds
	s_mov_b32 m0, s29
	s_nop 0
	buffer_load_dwordx4 v135, s[8:11], s56 offen lds
	s_mov_b32 m0, s30
	s_nop 0
	buffer_load_dwordx4 v137, s[8:11], s56 offen lds
	s_mov_b32 m0, s25
	s_nop 0
	buffer_load_dwordx4 v134, s[4:7], s55 offen lds
	s_mov_b32 m0, s31
	s_nop 0
	buffer_load_dwordx4 v136, s[4:7], s55 offen lds
	s_waitcnt vmcnt(8)
	s_waitcnt lgkmcnt(0)
	s_barrier
	s_waitcnt lgkmcnt(7)
	v_mfma_f32_16x16x32_bf16 v[62:65], v[140:143], v[172:175], v[62:65]
	v_mfma_f32_16x16x32_bf16 v[58:61], v[148:151], v[172:175], v[58:61]
	s_waitcnt lgkmcnt(5)
	v_mfma_f32_16x16x32_bf16 v[46:49], v[140:143], v[180:183], v[46:49]
	v_mfma_f32_16x16x32_bf16 v[42:45], v[148:151], v[180:183], v[42:45]
	s_waitcnt lgkmcnt(3)
	v_mfma_f32_16x16x32_bf16 v[30:33], v[140:143], v[188:191], v[30:33]
	v_mfma_f32_16x16x32_bf16 v[26:29], v[148:151], v[188:191], v[26:29]
	s_waitcnt lgkmcnt(1)
	v_mfma_f32_16x16x32_bf16 v[14:17], v[140:143], v[196:199], v[14:17]
	v_mfma_f32_16x16x32_bf16 v[10:13], v[148:151], v[196:199], v[10:13]
	v_mfma_f32_16x16x32_bf16 v[62:65], v[144:147], v[176:179], v[62:65]
	v_mfma_f32_16x16x32_bf16 v[58:61], v[152:155], v[176:179], v[58:61]
	v_mfma_f32_16x16x32_bf16 v[46:49], v[144:147], v[184:187], v[46:49]
	v_mfma_f32_16x16x32_bf16 v[42:45], v[152:155], v[184:187], v[42:45]
	v_mfma_f32_16x16x32_bf16 v[30:33], v[144:147], v[192:195], v[30:33]
	v_mfma_f32_16x16x32_bf16 v[26:29], v[152:155], v[192:195], v[26:29]
	s_waitcnt lgkmcnt(0)
	v_mfma_f32_16x16x32_bf16 v[14:17], v[144:147], v[200:203], v[14:17]
	v_mfma_f32_16x16x32_bf16 v[10:13], v[152:155], v[200:203], v[10:13]
	v_mfma_f32_16x16x32_bf16 v[54:57], v[156:159], v[172:175], v[54:57]
	v_mfma_f32_16x16x32_bf16 v[50:53], v[164:167], v[172:175], v[50:53]
	v_mfma_f32_16x16x32_bf16 v[38:41], v[156:159], v[180:183], v[38:41]
	v_mfma_f32_16x16x32_bf16 v[34:37], v[164:167], v[180:183], v[34:37]
	v_mfma_f32_16x16x32_bf16 v[22:25], v[156:159], v[188:191], v[22:25]
	v_mfma_f32_16x16x32_bf16 v[18:21], v[164:167], v[188:191], v[18:21]
	v_mfma_f32_16x16x32_bf16 v[6:9], v[156:159], v[196:199], v[6:9]
	v_mfma_f32_16x16x32_bf16 v[2:5], v[164:167], v[196:199], v[2:5]
	v_mfma_f32_16x16x32_bf16 v[54:57], v[160:163], v[176:179], v[54:57]
	v_mfma_f32_16x16x32_bf16 v[50:53], v[168:171], v[176:179], v[50:53]
	v_mfma_f32_16x16x32_bf16 v[38:41], v[160:163], v[184:187], v[38:41]
	v_mfma_f32_16x16x32_bf16 v[34:37], v[168:171], v[184:187], v[34:37]
	v_mfma_f32_16x16x32_bf16 v[22:25], v[160:163], v[192:195], v[22:25]
	v_mfma_f32_16x16x32_bf16 v[18:21], v[168:171], v[192:195], v[18:21]
	v_mfma_f32_16x16x32_bf16 v[6:9], v[160:163], v[200:203], v[6:9]
	v_mfma_f32_16x16x32_bf16 v[2:5], v[168:171], v[200:203], v[2:5]
	s_barrier
	v_add_u32_e32 v152, 0x18000, v138
	v_add_u32_e32 v168, 0x1c000, v138
	ds_read_b128 v[140:143], v152
	ds_read_b128 v[144:147], v152 offset:1024
	ds_read_b128 v[148:151], v152 offset:2048
	ds_read_b128 v[152:155], v152 offset:3072
	ds_read_b128 v[156:159], v168
	ds_read_b128 v[160:163], v168 offset:1024
	ds_read_b128 v[164:167], v168 offset:2048
	ds_read_b128 v[168:171], v168 offset:3072
	s_add_i32 s55, s55, 0x80000
	s_mov_b32 m0, s34
	ds_read_b128 v[172:175], v139 offset:32768
	ds_read_b128 v[176:179], v139 offset:33792
	ds_read_b128 v[180:183], v139 offset:34816
	ds_read_b128 v[184:187], v139 offset:35840
	ds_read_b128 v[188:191], v139 offset:36864
	ds_read_b128 v[192:195], v139 offset:37888
	ds_read_b128 v[196:199], v139 offset:38912
	ds_read_b128 v[200:203], v139 offset:39936
	buffer_load_dwordx4 v134, s[4:7], s55 offen lds
	s_mov_b32 m0, s35
	s_nop 0
	buffer_load_dwordx4 v136, s[4:7], s55 offen lds
	s_waitcnt vmcnt(8)
	s_waitcnt lgkmcnt(0)
	s_barrier
	s_waitcnt lgkmcnt(7)
	v_mfma_f32_16x16x32_bf16 v[126:129], v[140:143], v[172:175], v[126:129]
	v_mfma_f32_16x16x32_bf16 v[122:125], v[148:151], v[172:175], v[122:125]
	s_waitcnt lgkmcnt(5)
	v_mfma_f32_16x16x32_bf16 v[110:113], v[140:143], v[180:183], v[110:113]
	v_mfma_f32_16x16x32_bf16 v[106:109], v[148:151], v[180:183], v[106:109]
	s_waitcnt lgkmcnt(3)
	v_mfma_f32_16x16x32_bf16 v[98:101], v[140:143], v[188:191], v[98:101]
	v_mfma_f32_16x16x32_bf16 v[90:93], v[148:151], v[188:191], v[90:93]
	s_waitcnt lgkmcnt(1)
	v_mfma_f32_16x16x32_bf16 v[82:85], v[140:143], v[196:199], v[82:85]
	v_mfma_f32_16x16x32_bf16 v[74:77], v[148:151], v[196:199], v[74:77]
	v_mfma_f32_16x16x32_bf16 v[126:129], v[144:147], v[176:179], v[126:129]
	v_mfma_f32_16x16x32_bf16 v[122:125], v[152:155], v[176:179], v[122:125]
	v_mfma_f32_16x16x32_bf16 v[110:113], v[144:147], v[184:187], v[110:113]
	v_mfma_f32_16x16x32_bf16 v[106:109], v[152:155], v[184:187], v[106:109]
	v_mfma_f32_16x16x32_bf16 v[98:101], v[144:147], v[192:195], v[98:101]
	v_mfma_f32_16x16x32_bf16 v[90:93], v[152:155], v[192:195], v[90:93]
	s_waitcnt lgkmcnt(0)
	v_mfma_f32_16x16x32_bf16 v[82:85], v[144:147], v[200:203], v[82:85]
	v_mfma_f32_16x16x32_bf16 v[74:77], v[152:155], v[200:203], v[74:77]
	v_mfma_f32_16x16x32_bf16 v[118:121], v[156:159], v[172:175], v[118:121]
	v_mfma_f32_16x16x32_bf16 v[114:117], v[164:167], v[172:175], v[114:117]
	v_mfma_f32_16x16x32_bf16 v[102:105], v[156:159], v[180:183], v[102:105]
	v_mfma_f32_16x16x32_bf16 v[94:97], v[164:167], v[180:183], v[94:97]
	v_mfma_f32_16x16x32_bf16 v[86:89], v[156:159], v[188:191], v[86:89]
	v_mfma_f32_16x16x32_bf16 v[78:81], v[164:167], v[188:191], v[78:81]
	v_mfma_f32_16x16x32_bf16 v[70:73], v[156:159], v[196:199], v[70:73]
	v_mfma_f32_16x16x32_bf16 v[66:69], v[164:167], v[196:199], v[66:69]
	v_mfma_f32_16x16x32_bf16 v[118:121], v[160:163], v[176:179], v[118:121]
	v_mfma_f32_16x16x32_bf16 v[114:117], v[168:171], v[176:179], v[114:117]
	v_mfma_f32_16x16x32_bf16 v[102:105], v[160:163], v[184:187], v[102:105]
	v_mfma_f32_16x16x32_bf16 v[94:97], v[168:171], v[184:187], v[94:97]
	v_mfma_f32_16x16x32_bf16 v[86:89], v[160:163], v[192:195], v[86:89]
	v_mfma_f32_16x16x32_bf16 v[78:81], v[168:171], v[192:195], v[78:81]
	v_mfma_f32_16x16x32_bf16 v[70:73], v[160:163], v[200:203], v[70:73]
	v_mfma_f32_16x16x32_bf16 v[66:69], v[168:171], v[200:203], v[66:69]
	s_barrier
	s_mov_b32 m0, s36
	s_or_b32 s55, s54, 0x80
	ds_read_b128 v[172:175], v139 offset:49152
	ds_read_b128 v[176:179], v139 offset:50176
	ds_read_b128 v[180:183], v139 offset:51200
	ds_read_b128 v[184:187], v139 offset:52224
	ds_read_b128 v[188:191], v139 offset:53248
	ds_read_b128 v[192:195], v139 offset:54272
	ds_read_b128 v[196:199], v139 offset:55296
	ds_read_b128 v[200:203], v139 offset:56320
	buffer_load_dwordx4 v135, s[8:11], s55 offen lds
	s_mov_b32 m0, s37
	s_add_i32 s54, s54, 0x80080
	buffer_load_dwordx4 v137, s[8:11], s55 offen lds
	s_mov_b32 m0, s41
	s_nop 0
	buffer_load_dwordx4 v135, s[8:11], s54 offen lds
	s_mov_b32 m0, s42
	s_nop 0
	buffer_load_dwordx4 v137, s[8:11], s54 offen lds
	s_mov_b32 m0, s38
	s_nop 0
	buffer_load_dwordx4 v134, s[4:7], s53 offen lds
	s_mov_b32 m0, s40
	s_nop 0
	buffer_load_dwordx4 v136, s[4:7], s53 offen lds
	s_waitcnt vmcnt(8)
	s_waitcnt lgkmcnt(0)
	s_barrier
	s_waitcnt lgkmcnt(7)
	v_mfma_f32_16x16x32_bf16 v[62:65], v[140:143], v[172:175], v[62:65]
	v_mfma_f32_16x16x32_bf16 v[58:61], v[148:151], v[172:175], v[58:61]
	s_waitcnt lgkmcnt(5)
	v_mfma_f32_16x16x32_bf16 v[46:49], v[140:143], v[180:183], v[46:49]
	v_mfma_f32_16x16x32_bf16 v[42:45], v[148:151], v[180:183], v[42:45]
	s_waitcnt lgkmcnt(3)
	v_mfma_f32_16x16x32_bf16 v[30:33], v[140:143], v[188:191], v[30:33]
	v_mfma_f32_16x16x32_bf16 v[26:29], v[148:151], v[188:191], v[26:29]
	s_waitcnt lgkmcnt(1)
	v_mfma_f32_16x16x32_bf16 v[14:17], v[140:143], v[196:199], v[14:17]
	v_mfma_f32_16x16x32_bf16 v[10:13], v[148:151], v[196:199], v[10:13]
	v_mfma_f32_16x16x32_bf16 v[62:65], v[144:147], v[176:179], v[62:65]
	v_mfma_f32_16x16x32_bf16 v[58:61], v[152:155], v[176:179], v[58:61]
	v_mfma_f32_16x16x32_bf16 v[46:49], v[144:147], v[184:187], v[46:49]
	v_mfma_f32_16x16x32_bf16 v[42:45], v[152:155], v[184:187], v[42:45]
	v_mfma_f32_16x16x32_bf16 v[30:33], v[144:147], v[192:195], v[30:33]
	v_mfma_f32_16x16x32_bf16 v[26:29], v[152:155], v[192:195], v[26:29]
	s_waitcnt lgkmcnt(0)
	v_mfma_f32_16x16x32_bf16 v[14:17], v[144:147], v[200:203], v[14:17]
	v_mfma_f32_16x16x32_bf16 v[10:13], v[152:155], v[200:203], v[10:13]
	v_mfma_f32_16x16x32_bf16 v[54:57], v[156:159], v[172:175], v[54:57]
	v_mfma_f32_16x16x32_bf16 v[50:53], v[164:167], v[172:175], v[50:53]
	v_mfma_f32_16x16x32_bf16 v[38:41], v[156:159], v[180:183], v[38:41]
	v_mfma_f32_16x16x32_bf16 v[34:37], v[164:167], v[180:183], v[34:37]
	v_mfma_f32_16x16x32_bf16 v[22:25], v[156:159], v[188:191], v[22:25]
	v_mfma_f32_16x16x32_bf16 v[18:21], v[164:167], v[188:191], v[18:21]
	v_mfma_f32_16x16x32_bf16 v[6:9], v[156:159], v[196:199], v[6:9]
	v_mfma_f32_16x16x32_bf16 v[2:5], v[164:167], v[196:199], v[2:5]
	v_mfma_f32_16x16x32_bf16 v[54:57], v[160:163], v[176:179], v[54:57]
	v_mfma_f32_16x16x32_bf16 v[50:53], v[168:171], v[176:179], v[50:53]
	v_mfma_f32_16x16x32_bf16 v[38:41], v[160:163], v[184:187], v[38:41]
	v_mfma_f32_16x16x32_bf16 v[34:37], v[168:171], v[184:187], v[34:37]
	v_mfma_f32_16x16x32_bf16 v[22:25], v[160:163], v[192:195], v[22:25]
	v_mfma_f32_16x16x32_bf16 v[18:21], v[168:171], v[192:195], v[18:21]
	v_mfma_f32_16x16x32_bf16 v[6:9], v[160:163], v[200:203], v[6:9]
	v_mfma_f32_16x16x32_bf16 v[2:5], v[168:171], v[200:203], v[2:5]
	s_barrier
	s_add_i32 s51, s51, 2
	s_addk_i32 s52, 0x100
	s_cmp_gt_u32 s51, 29
	s_cbranch_scc0 .LBB0_686
	s_andn2_b64 vcc, exec, s[2:3]
	s_cbranch_vccnz .LBB0_678
	v_mov_b32_e32 v2, 0
	s_mov_b32 s14, s46
	s_mov_b32 s15, s47
	s_mov_b32 s27, s48
	s_mov_b32 s33, s13
	s_mov_b32 s45, s12
	v_mov_b32_e32 v3, v2
	v_mov_b32_e32 v4, v2
	v_mov_b32_e32 v5, v2
	v_mov_b32_e32 v6, v2
	v_mov_b32_e32 v7, v2
	v_mov_b32_e32 v8, v2
	v_mov_b32_e32 v9, v2
	v_mov_b32_e32 v18, v2
	v_mov_b32_e32 v19, v2
	v_mov_b32_e32 v20, v2
	v_mov_b32_e32 v21, v2
	v_mov_b32_e32 v22, v2
	v_mov_b32_e32 v23, v2
	v_mov_b32_e32 v24, v2
	v_mov_b32_e32 v25, v2
	v_mov_b32_e32 v34, v2
	v_mov_b32_e32 v35, v2
	v_mov_b32_e32 v36, v2
	v_mov_b32_e32 v37, v2
	v_mov_b32_e32 v38, v2
	v_mov_b32_e32 v39, v2
	v_mov_b32_e32 v40, v2
	v_mov_b32_e32 v41, v2
	v_mov_b32_e32 v50, v2
	v_mov_b32_e32 v51, v2
	v_mov_b32_e32 v52, v2
	v_mov_b32_e32 v53, v2
	v_mov_b32_e32 v54, v2
	v_mov_b32_e32 v55, v2
	v_mov_b32_e32 v56, v2
	v_mov_b32_e32 v57, v2
	v_mov_b32_e32 v10, v2
	v_mov_b32_e32 v11, v2
	v_mov_b32_e32 v12, v2
	v_mov_b32_e32 v13, v2
	v_mov_b32_e32 v14, v2
	v_mov_b32_e32 v15, v2
	v_mov_b32_e32 v16, v2
	v_mov_b32_e32 v17, v2
	v_mov_b32_e32 v26, v2
	v_mov_b32_e32 v27, v2
	v_mov_b32_e32 v28, v2
	v_mov_b32_e32 v29, v2
	v_mov_b32_e32 v30, v2
	v_mov_b32_e32 v31, v2
	v_mov_b32_e32 v32, v2
	v_mov_b32_e32 v33, v2
	v_mov_b32_e32 v42, v2
	v_mov_b32_e32 v43, v2
	v_mov_b32_e32 v44, v2
	v_mov_b32_e32 v45, v2
	v_mov_b32_e32 v46, v2
	v_mov_b32_e32 v47, v2
	v_mov_b32_e32 v48, v2
	v_mov_b32_e32 v49, v2
	v_mov_b32_e32 v58, v2
	v_mov_b32_e32 v59, v2
	v_mov_b32_e32 v60, v2
	v_mov_b32_e32 v61, v2
	v_mov_b32_e32 v62, v2
	v_mov_b32_e32 v63, v2
	v_mov_b32_e32 v64, v2
	v_mov_b32_e32 v65, v2
	v_mov_b32_e32 v66, v2
	v_mov_b32_e32 v67, v2
	v_mov_b32_e32 v68, v2
	v_mov_b32_e32 v69, v2
	v_mov_b32_e32 v70, v2
	v_mov_b32_e32 v71, v2
	v_mov_b32_e32 v72, v2
	v_mov_b32_e32 v73, v2
	v_mov_b32_e32 v78, v2
	v_mov_b32_e32 v79, v2
	v_mov_b32_e32 v80, v2
	v_mov_b32_e32 v81, v2
	v_mov_b32_e32 v86, v2
	v_mov_b32_e32 v87, v2
	v_mov_b32_e32 v88, v2
	v_mov_b32_e32 v89, v2
	v_mov_b32_e32 v94, v2
	v_mov_b32_e32 v95, v2
	v_mov_b32_e32 v96, v2
	v_mov_b32_e32 v97, v2
	v_mov_b32_e32 v102, v2
	v_mov_b32_e32 v103, v2
	v_mov_b32_e32 v104, v2
	v_mov_b32_e32 v105, v2
	v_mov_b32_e32 v114, v2
	v_mov_b32_e32 v115, v2
	v_mov_b32_e32 v116, v2
	v_mov_b32_e32 v117, v2
	v_mov_b32_e32 v118, v2
	v_mov_b32_e32 v119, v2
	v_mov_b32_e32 v120, v2
	v_mov_b32_e32 v121, v2
	v_mov_b32_e32 v74, v2
	v_mov_b32_e32 v75, v2
	v_mov_b32_e32 v76, v2
	v_mov_b32_e32 v77, v2
	v_mov_b32_e32 v82, v2
	v_mov_b32_e32 v83, v2
	v_mov_b32_e32 v84, v2
	v_mov_b32_e32 v85, v2
	v_mov_b32_e32 v90, v2
	v_mov_b32_e32 v91, v2
	v_mov_b32_e32 v92, v2
	v_mov_b32_e32 v93, v2
	v_mov_b32_e32 v98, v2
	v_mov_b32_e32 v99, v2
	v_mov_b32_e32 v100, v2
	v_mov_b32_e32 v101, v2
	v_mov_b32_e32 v106, v2
	v_mov_b32_e32 v107, v2
	v_mov_b32_e32 v108, v2
	v_mov_b32_e32 v109, v2
	v_mov_b32_e32 v110, v2
	v_mov_b32_e32 v111, v2
	v_mov_b32_e32 v112, v2
	v_mov_b32_e32 v113, v2
	v_mov_b32_e32 v122, v2
	v_mov_b32_e32 v123, v2
	v_mov_b32_e32 v124, v2
	v_mov_b32_e32 v125, v2
	v_mov_b32_e32 v126, v2
	v_mov_b32_e32 v127, v2
	v_mov_b32_e32 v128, v2
	v_mov_b32_e32 v129, v2
	s_branch .LBB0_678

.LBB0_907:
	v_add_u32_e32 v166, 0x10000, v179
	ds_read_b128 v[162:165], v166
	ds_read_b128 v[182:185], v166 offset:1024
	ds_read_b128 v[186:189], v166 offset:2048
	ds_read_b128 v[190:193], v166 offset:3072
	v_add_u32_e32 v166, 0x14000, v179
	ds_read_b128 v[194:197], v166
	ds_read_b128 v[198:201], v166 offset:1024
	ds_read_b128 v[202:205], v166 offset:2048
	ds_read_b128 v[206:209], v166 offset:3072
	s_add_i32 s10, s45, s64
	s_add_i32 s26, s40, s64
	s_add_i32 s11, s10, 0x1000
	s_addk_i32 s26, 0x1000
	s_cmp_eq_u32 s64, 0
	s_cselect_b32 s29, s62, s11
	s_cselect_b32 s27, s63, s26
	s_add_i32 s26, s29, 0x80
	s_add_i32 s28, s27, 0x80
	s_add_i32 s10, s10, 0x80f80
	s_mov_b32 m0, s55
	ds_read_b128 v[210:213], v180
	ds_read_b128 v[214:217], v180 offset:1024
	ds_read_b128 v[218:221], v180 offset:2048
	ds_read_b128 v[222:225], v180 offset:3072
	ds_read_b128 v[226:229], v180 offset:4096
	ds_read_b128 v[230:233], v180 offset:5120
	ds_read_b128 v[234:237], v180 offset:6144
	ds_read_b128 v[238:241], v180 offset:7168
	buffer_load_dwordx4 v1, s[4:7], s10 offen lds
	s_mov_b32 m0, s56
	s_nop 0
	buffer_load_dwordx4 v175, s[4:7], s10 offen lds
	s_waitcnt vmcnt(8)
	s_waitcnt lgkmcnt(0)
	s_barrier
	s_waitcnt lgkmcnt(7)
	v_mfma_f32_16x16x32_bf16 v[126:129], v[162:165], v[210:213], v[126:129]
	v_mfma_f32_16x16x32_bf16 v[122:125], v[186:189], v[210:213], v[122:125]
	s_waitcnt lgkmcnt(5)
	v_mfma_f32_16x16x32_bf16 v[118:121], v[162:165], v[218:221], v[118:121]
	v_mfma_f32_16x16x32_bf16 v[114:117], v[186:189], v[218:221], v[114:117]
	s_waitcnt lgkmcnt(3)
	v_mfma_f32_16x16x32_bf16 v[110:113], v[162:165], v[226:229], v[110:113]
	v_mfma_f32_16x16x32_bf16 v[106:109], v[186:189], v[226:229], v[106:109]
	s_waitcnt lgkmcnt(1)
	v_mfma_f32_16x16x32_bf16 v[102:105], v[162:165], v[234:237], v[102:105]
	v_mfma_f32_16x16x32_bf16 v[98:101], v[186:189], v[234:237], v[98:101]
	v_mfma_f32_16x16x32_bf16 v[126:129], v[182:185], v[214:217], v[126:129]
	v_mfma_f32_16x16x32_bf16 v[122:125], v[190:193], v[214:217], v[122:125]
	v_mfma_f32_16x16x32_bf16 v[118:121], v[182:185], v[222:225], v[118:121]
	v_mfma_f32_16x16x32_bf16 v[114:117], v[190:193], v[222:225], v[114:117]
	v_mfma_f32_16x16x32_bf16 v[110:113], v[182:185], v[230:233], v[110:113]
	v_mfma_f32_16x16x32_bf16 v[106:109], v[190:193], v[230:233], v[106:109]
	s_waitcnt lgkmcnt(0)
	v_mfma_f32_16x16x32_bf16 v[102:105], v[182:185], v[238:241], v[102:105]
	v_mfma_f32_16x16x32_bf16 v[98:101], v[190:193], v[238:241], v[98:101]
	v_mfma_f32_16x16x32_bf16 v[94:97], v[194:197], v[210:213], v[94:97]
	v_mfma_f32_16x16x32_bf16 v[90:93], v[202:205], v[210:213], v[90:93]
	v_mfma_f32_16x16x32_bf16 v[86:89], v[194:197], v[218:221], v[86:89]
	v_mfma_f32_16x16x32_bf16 v[82:85], v[202:205], v[218:221], v[82:85]
	v_mfma_f32_16x16x32_bf16 v[78:81], v[194:197], v[226:229], v[78:81]
	v_mfma_f32_16x16x32_bf16 v[74:77], v[202:205], v[226:229], v[74:77]
	v_mfma_f32_16x16x32_bf16 v[70:73], v[194:197], v[234:237], v[70:73]
	v_mfma_f32_16x16x32_bf16 v[66:69], v[202:205], v[234:237], v[66:69]
	v_mfma_f32_16x16x32_bf16 v[94:97], v[198:201], v[214:217], v[94:97]
	v_mfma_f32_16x16x32_bf16 v[90:93], v[206:209], v[214:217], v[90:93]
	v_mfma_f32_16x16x32_bf16 v[86:89], v[198:201], v[222:225], v[86:89]
	v_mfma_f32_16x16x32_bf16 v[82:85], v[206:209], v[222:225], v[82:85]
	v_mfma_f32_16x16x32_bf16 v[78:81], v[198:201], v[230:233], v[78:81]
	v_mfma_f32_16x16x32_bf16 v[74:77], v[206:209], v[230:233], v[74:77]
	v_mfma_f32_16x16x32_bf16 v[70:73], v[198:201], v[238:241], v[70:73]
	v_mfma_f32_16x16x32_bf16 v[66:69], v[206:209], v[238:241], v[66:69]
	s_barrier
	s_mov_b32 m0, s37
	s_mov_b32 s10, s6
	s_mov_b32 s11, s7
	ds_read_b128 v[210:213], v180 offset:16384
	ds_read_b128 v[214:217], v180 offset:17408
	ds_read_b128 v[218:221], v180 offset:18432
	ds_read_b128 v[222:225], v180 offset:19456
	ds_read_b128 v[226:229], v180 offset:20480
	ds_read_b128 v[230:233], v180 offset:21504
	ds_read_b128 v[234:237], v180 offset:22528
	ds_read_b128 v[238:241], v180 offset:23552
	buffer_load_dwordx4 v174, s[8:11], s27 offen lds
	s_mov_b32 m0, s38
	s_add_i32 s66, s27, 0x80000
	buffer_load_dwordx4 v176, s[8:11], s27 offen lds
	s_mov_b32 m0, s39
	s_nop 0
	buffer_load_dwordx4 v174, s[8:11], s66 offen lds
	s_mov_b32 m0, s41
	s_nop 0
	buffer_load_dwordx4 v176, s[8:11], s66 offen lds
	s_mov_b32 m0, s36
	s_nop 0
	buffer_load_dwordx4 v1, s[4:7], s29 offen lds
	s_mov_b32 m0, s42
	s_nop 0
	buffer_load_dwordx4 v175, s[4:7], s29 offen lds
	s_waitcnt vmcnt(8)
	s_waitcnt lgkmcnt(0)
	s_barrier
	s_waitcnt lgkmcnt(7)
	v_mfma_f32_16x16x32_bf16 v[62:65], v[162:165], v[210:213], v[62:65]
	v_mfma_f32_16x16x32_bf16 v[58:61], v[186:189], v[210:213], v[58:61]
	s_waitcnt lgkmcnt(5)
	v_mfma_f32_16x16x32_bf16 v[54:57], v[162:165], v[218:221], v[54:57]
	v_mfma_f32_16x16x32_bf16 v[50:53], v[186:189], v[218:221], v[50:53]
	s_waitcnt lgkmcnt(3)
	v_mfma_f32_16x16x32_bf16 v[46:49], v[162:165], v[226:229], v[46:49]
	v_mfma_f32_16x16x32_bf16 v[42:45], v[186:189], v[226:229], v[42:45]
	s_waitcnt lgkmcnt(1)
	v_mfma_f32_16x16x32_bf16 v[38:41], v[162:165], v[234:237], v[38:41]
	v_mfma_f32_16x16x32_bf16 v[34:37], v[186:189], v[234:237], v[34:37]
	v_mfma_f32_16x16x32_bf16 v[62:65], v[182:185], v[214:217], v[62:65]
	v_mfma_f32_16x16x32_bf16 v[58:61], v[190:193], v[214:217], v[58:61]
	v_mfma_f32_16x16x32_bf16 v[54:57], v[182:185], v[222:225], v[54:57]
	v_mfma_f32_16x16x32_bf16 v[50:53], v[190:193], v[222:225], v[50:53]
	v_mfma_f32_16x16x32_bf16 v[46:49], v[182:185], v[230:233], v[46:49]
	v_mfma_f32_16x16x32_bf16 v[42:45], v[190:193], v[230:233], v[42:45]
	s_waitcnt lgkmcnt(0)
	v_mfma_f32_16x16x32_bf16 v[38:41], v[182:185], v[238:241], v[38:41]
	v_mfma_f32_16x16x32_bf16 v[34:37], v[190:193], v[238:241], v[34:37]
	v_mfma_f32_16x16x32_bf16 v[30:33], v[194:197], v[210:213], v[30:33]
	v_mfma_f32_16x16x32_bf16 v[26:29], v[202:205], v[210:213], v[26:29]
	v_mfma_f32_16x16x32_bf16 v[22:25], v[194:197], v[218:221], v[22:25]
	v_mfma_f32_16x16x32_bf16 v[18:21], v[202:205], v[218:221], v[18:21]
	v_mfma_f32_16x16x32_bf16 v[14:17], v[194:197], v[226:229], v[14:17]
	v_mfma_f32_16x16x32_bf16 v[10:13], v[202:205], v[226:229], v[10:13]
	v_mfma_f32_16x16x32_bf16 v[6:9], v[194:197], v[234:237], v[6:9]
	v_mfma_f32_16x16x32_bf16 v[2:5], v[202:205], v[234:237], v[2:5]
	v_mfma_f32_16x16x32_bf16 v[30:33], v[198:201], v[214:217], v[30:33]
	v_mfma_f32_16x16x32_bf16 v[26:29], v[206:209], v[214:217], v[26:29]
	v_mfma_f32_16x16x32_bf16 v[22:25], v[198:201], v[222:225], v[22:25]
	v_mfma_f32_16x16x32_bf16 v[18:21], v[206:209], v[222:225], v[18:21]
	v_mfma_f32_16x16x32_bf16 v[14:17], v[198:201], v[230:233], v[14:17]
	v_mfma_f32_16x16x32_bf16 v[10:13], v[206:209], v[230:233], v[10:13]
	v_mfma_f32_16x16x32_bf16 v[6:9], v[198:201], v[238:241], v[6:9]
	v_mfma_f32_16x16x32_bf16 v[2:5], v[206:209], v[238:241], v[2:5]
	s_barrier
	v_add_u32_e32 v166, 0x18000, v179
	ds_read_b128 v[162:165], v166
	ds_read_b128 v[182:185], v166 offset:1024
	ds_read_b128 v[186:189], v166 offset:2048
	ds_read_b128 v[190:193], v166 offset:3072
	v_add_u32_e32 v166, 0x1c000, v179
	ds_read_b128 v[194:197], v166
	ds_read_b128 v[198:201], v166 offset:1024
	ds_read_b128 v[202:205], v166 offset:2048
	ds_read_b128 v[206:209], v166 offset:3072
	s_add_i32 s29, s29, 0x80000
	s_mov_b32 m0, s43
	ds_read_b128 v[210:213], v180 offset:32768
	ds_read_b128 v[214:217], v180 offset:33792
	ds_read_b128 v[218:221], v180 offset:34816
	ds_read_b128 v[222:225], v180 offset:35840
	ds_read_b128 v[226:229], v180 offset:36864
	ds_read_b128 v[230:233], v180 offset:37888
	ds_read_b128 v[234:237], v180 offset:38912
	ds_read_b128 v[238:241], v180 offset:39936
	buffer_load_dwordx4 v1, s[4:7], s29 offen lds
	s_mov_b32 m0, s44
	s_nop 0
	buffer_load_dwordx4 v175, s[4:7], s29 offen lds
	s_waitcnt vmcnt(8)
	s_waitcnt lgkmcnt(0)
	s_barrier
	s_waitcnt lgkmcnt(7)
	v_mfma_f32_16x16x32_bf16 v[126:129], v[162:165], v[210:213], v[126:129]
	v_mfma_f32_16x16x32_bf16 v[122:125], v[186:189], v[210:213], v[122:125]
	s_waitcnt lgkmcnt(5)
	v_mfma_f32_16x16x32_bf16 v[118:121], v[162:165], v[218:221], v[118:121]
	v_mfma_f32_16x16x32_bf16 v[114:117], v[186:189], v[218:221], v[114:117]
	s_waitcnt lgkmcnt(3)
	v_mfma_f32_16x16x32_bf16 v[110:113], v[162:165], v[226:229], v[110:113]
	v_mfma_f32_16x16x32_bf16 v[106:109], v[186:189], v[226:229], v[106:109]
	s_waitcnt lgkmcnt(1)
	v_mfma_f32_16x16x32_bf16 v[102:105], v[162:165], v[234:237], v[102:105]
	v_mfma_f32_16x16x32_bf16 v[98:101], v[186:189], v[234:237], v[98:101]
	v_mfma_f32_16x16x32_bf16 v[126:129], v[182:185], v[214:217], v[126:129]
	v_mfma_f32_16x16x32_bf16 v[122:125], v[190:193], v[214:217], v[122:125]
	v_mfma_f32_16x16x32_bf16 v[118:121], v[182:185], v[222:225], v[118:121]
	v_mfma_f32_16x16x32_bf16 v[114:117], v[190:193], v[222:225], v[114:117]
	v_mfma_f32_16x16x32_bf16 v[110:113], v[182:185], v[230:233], v[110:113]
	v_mfma_f32_16x16x32_bf16 v[106:109], v[190:193], v[230:233], v[106:109]
	s_waitcnt lgkmcnt(0)
	v_mfma_f32_16x16x32_bf16 v[102:105], v[182:185], v[238:241], v[102:105]
	v_mfma_f32_16x16x32_bf16 v[98:101], v[190:193], v[238:241], v[98:101]
	v_mfma_f32_16x16x32_bf16 v[94:97], v[194:197], v[210:213], v[94:97]
	v_mfma_f32_16x16x32_bf16 v[90:93], v[202:205], v[210:213], v[90:93]
	v_mfma_f32_16x16x32_bf16 v[86:89], v[194:197], v[218:221], v[86:89]
	v_mfma_f32_16x16x32_bf16 v[82:85], v[202:205], v[218:221], v[82:85]
	v_mfma_f32_16x16x32_bf16 v[78:81], v[194:197], v[226:229], v[78:81]
	v_mfma_f32_16x16x32_bf16 v[74:77], v[202:205], v[226:229], v[74:77]
	v_mfma_f32_16x16x32_bf16 v[70:73], v[194:197], v[234:237], v[70:73]
	v_mfma_f32_16x16x32_bf16 v[66:69], v[202:205], v[234:237], v[66:69]
	v_mfma_f32_16x16x32_bf16 v[94:97], v[198:201], v[214:217], v[94:97]
	v_mfma_f32_16x16x32_bf16 v[90:93], v[206:209], v[214:217], v[90:93]
	v_mfma_f32_16x16x32_bf16 v[86:89], v[198:201], v[222:225], v[86:89]
	v_mfma_f32_16x16x32_bf16 v[82:85], v[206:209], v[222:225], v[82:85]
	v_mfma_f32_16x16x32_bf16 v[78:81], v[198:201], v[230:233], v[78:81]
	v_mfma_f32_16x16x32_bf16 v[74:77], v[206:209], v[230:233], v[74:77]
	v_mfma_f32_16x16x32_bf16 v[70:73], v[198:201], v[238:241], v[70:73]
	v_mfma_f32_16x16x32_bf16 v[66:69], v[206:209], v[238:241], v[66:69]
	s_barrier
	s_mov_b32 m0, s49
	ds_read_b128 v[210:213], v180 offset:49152
	ds_read_b128 v[214:217], v180 offset:50176
	ds_read_b128 v[218:221], v180 offset:51200
	ds_read_b128 v[222:225], v180 offset:52224
	ds_read_b128 v[226:229], v180 offset:53248
	ds_read_b128 v[230:233], v180 offset:54272
	ds_read_b128 v[234:237], v180 offset:55296
	ds_read_b128 v[238:241], v180 offset:56320
	buffer_load_dwordx4 v174, s[8:11], s28 offen lds
	s_mov_b32 m0, s50
	s_add_i32 s27, s27, 0x80080
	buffer_load_dwordx4 v176, s[8:11], s28 offen lds
	s_mov_b32 m0, s53
	s_nop 0
	buffer_load_dwordx4 v174, s[8:11], s27 offen lds
	s_mov_b32 m0, s54
	s_nop 0
	buffer_load_dwordx4 v176, s[8:11], s27 offen lds
	s_mov_b32 m0, s51
	s_nop 0
	buffer_load_dwordx4 v1, s[4:7], s26 offen lds
	s_mov_b32 m0, s52
	s_nop 0
	buffer_load_dwordx4 v175, s[4:7], s26 offen lds
	s_waitcnt vmcnt(8)
	s_waitcnt lgkmcnt(0)
	s_barrier
	s_waitcnt lgkmcnt(7)
	v_mfma_f32_16x16x32_bf16 v[62:65], v[162:165], v[210:213], v[62:65]
	v_mfma_f32_16x16x32_bf16 v[58:61], v[186:189], v[210:213], v[58:61]
	s_waitcnt lgkmcnt(5)
	v_mfma_f32_16x16x32_bf16 v[54:57], v[162:165], v[218:221], v[54:57]
	v_mfma_f32_16x16x32_bf16 v[50:53], v[186:189], v[218:221], v[50:53]
	s_waitcnt lgkmcnt(3)
	v_mfma_f32_16x16x32_bf16 v[46:49], v[162:165], v[226:229], v[46:49]
	v_mfma_f32_16x16x32_bf16 v[42:45], v[186:189], v[226:229], v[42:45]
	s_waitcnt lgkmcnt(1)
	v_mfma_f32_16x16x32_bf16 v[38:41], v[162:165], v[234:237], v[38:41]
	v_mfma_f32_16x16x32_bf16 v[34:37], v[186:189], v[234:237], v[34:37]
	v_mfma_f32_16x16x32_bf16 v[62:65], v[182:185], v[214:217], v[62:65]
	v_mfma_f32_16x16x32_bf16 v[58:61], v[190:193], v[214:217], v[58:61]
	v_mfma_f32_16x16x32_bf16 v[54:57], v[182:185], v[222:225], v[54:57]
	v_mfma_f32_16x16x32_bf16 v[50:53], v[190:193], v[222:225], v[50:53]
	v_mfma_f32_16x16x32_bf16 v[46:49], v[182:185], v[230:233], v[46:49]
	v_mfma_f32_16x16x32_bf16 v[42:45], v[190:193], v[230:233], v[42:45]
	s_waitcnt lgkmcnt(0)
	v_mfma_f32_16x16x32_bf16 v[38:41], v[182:185], v[238:241], v[38:41]
	v_mfma_f32_16x16x32_bf16 v[34:37], v[190:193], v[238:241], v[34:37]
	v_mfma_f32_16x16x32_bf16 v[30:33], v[194:197], v[210:213], v[30:33]
	v_mfma_f32_16x16x32_bf16 v[26:29], v[202:205], v[210:213], v[26:29]
	v_mfma_f32_16x16x32_bf16 v[22:25], v[194:197], v[218:221], v[22:25]
	v_mfma_f32_16x16x32_bf16 v[18:21], v[202:205], v[218:221], v[18:21]
	v_mfma_f32_16x16x32_bf16 v[14:17], v[194:197], v[226:229], v[14:17]
	v_mfma_f32_16x16x32_bf16 v[10:13], v[202:205], v[226:229], v[10:13]
	v_mfma_f32_16x16x32_bf16 v[6:9], v[194:197], v[234:237], v[6:9]
	v_mfma_f32_16x16x32_bf16 v[2:5], v[202:205], v[234:237], v[2:5]
	v_mfma_f32_16x16x32_bf16 v[30:33], v[198:201], v[214:217], v[30:33]
	v_mfma_f32_16x16x32_bf16 v[26:29], v[206:209], v[214:217], v[26:29]
	v_mfma_f32_16x16x32_bf16 v[22:25], v[198:201], v[222:225], v[22:25]
	v_mfma_f32_16x16x32_bf16 v[18:21], v[206:209], v[222:225], v[18:21]
	v_mfma_f32_16x16x32_bf16 v[14:17], v[198:201], v[230:233], v[14:17]
	v_mfma_f32_16x16x32_bf16 v[10:13], v[206:209], v[230:233], v[10:13]
	v_mfma_f32_16x16x32_bf16 v[6:9], v[198:201], v[238:241], v[6:9]
	v_mfma_f32_16x16x32_bf16 v[2:5], v[206:209], v[238:241], v[2:5]
	s_barrier
	s_add_i32 s10, s65, 2
	s_addk_i32 s64, 0x100
	s_cmp_gt_u32 s65, 29
	s_cbranch_scc1 .LBB0_910
	s_mov_b32 s65, s10
	s_branch .LBB0_869

.LBB0_1029:
	v_add_u32_e32 v152, 0x10000, v138
	v_add_u32_e32 v168, 0x14000, v138
	ds_read_b128 v[140:143], v152
	ds_read_b128 v[144:147], v152 offset:1024
	ds_read_b128 v[148:151], v152 offset:2048
	ds_read_b128 v[152:155], v152 offset:3072
	ds_read_b128 v[156:159], v168
	ds_read_b128 v[160:163], v168 offset:1024
	ds_read_b128 v[164:167], v168 offset:2048
	ds_read_b128 v[168:171], v168 offset:3072
	s_add_i32 s10, s30, s50
	s_add_i32 s51, s25, s50
	s_add_i32 s11, s10, 0x4000
	s_addk_i32 s51, 0x4000
	s_cmp_eq_u32 s50, 0
	s_cselect_b32 s53, s47, s11
	s_cselect_b32 s52, s48, s51
	s_or_b32 s51, s53, 0x80
	s_add_i32 s10, s10, 0x203f80
	s_mov_b32 m0, s41
	ds_read_b128 v[172:175], v139
	ds_read_b128 v[176:179], v139 offset:1024
	ds_read_b128 v[180:183], v139 offset:2048
	ds_read_b128 v[184:187], v139 offset:3072
	ds_read_b128 v[188:191], v139 offset:4096
	ds_read_b128 v[192:195], v139 offset:5120
	ds_read_b128 v[196:199], v139 offset:6144
	ds_read_b128 v[200:203], v139 offset:7168
	buffer_load_dwordx4 v134, s[4:7], s10 offen lds
	s_mov_b32 m0, s42
	s_nop 0
	buffer_load_dwordx4 v136, s[4:7], s10 offen lds
	s_waitcnt vmcnt(8)
	s_waitcnt lgkmcnt(0)
	s_barrier
	s_waitcnt lgkmcnt(7)
	v_mfma_f32_16x16x32_bf16 v[126:129], v[140:143], v[172:175], v[126:129]
	v_mfma_f32_16x16x32_bf16 v[122:125], v[148:151], v[172:175], v[122:125]
	s_waitcnt lgkmcnt(5)
	v_mfma_f32_16x16x32_bf16 v[114:117], v[140:143], v[180:183], v[114:117]
	v_mfma_f32_16x16x32_bf16 v[106:109], v[148:151], v[180:183], v[106:109]
	s_waitcnt lgkmcnt(3)
	v_mfma_f32_16x16x32_bf16 v[98:101], v[140:143], v[188:191], v[98:101]
	v_mfma_f32_16x16x32_bf16 v[90:93], v[148:151], v[188:191], v[90:93]
	s_waitcnt lgkmcnt(1)
	v_mfma_f32_16x16x32_bf16 v[82:85], v[140:143], v[196:199], v[82:85]
	v_mfma_f32_16x16x32_bf16 v[74:77], v[148:151], v[196:199], v[74:77]
	v_mfma_f32_16x16x32_bf16 v[126:129], v[144:147], v[176:179], v[126:129]
	v_mfma_f32_16x16x32_bf16 v[122:125], v[152:155], v[176:179], v[122:125]
	v_mfma_f32_16x16x32_bf16 v[114:117], v[144:147], v[184:187], v[114:117]
	v_mfma_f32_16x16x32_bf16 v[106:109], v[152:155], v[184:187], v[106:109]
	v_mfma_f32_16x16x32_bf16 v[98:101], v[144:147], v[192:195], v[98:101]
	v_mfma_f32_16x16x32_bf16 v[90:93], v[152:155], v[192:195], v[90:93]
	s_waitcnt lgkmcnt(0)
	v_mfma_f32_16x16x32_bf16 v[82:85], v[144:147], v[200:203], v[82:85]
	v_mfma_f32_16x16x32_bf16 v[74:77], v[152:155], v[200:203], v[74:77]
	v_mfma_f32_16x16x32_bf16 v[118:121], v[156:159], v[172:175], v[118:121]
	v_mfma_f32_16x16x32_bf16 v[110:113], v[164:167], v[172:175], v[110:113]
	v_mfma_f32_16x16x32_bf16 v[102:105], v[156:159], v[180:183], v[102:105]
	v_mfma_f32_16x16x32_bf16 v[94:97], v[164:167], v[180:183], v[94:97]
	v_mfma_f32_16x16x32_bf16 v[86:89], v[156:159], v[188:191], v[86:89]
	v_mfma_f32_16x16x32_bf16 v[78:81], v[164:167], v[188:191], v[78:81]
	v_mfma_f32_16x16x32_bf16 v[70:73], v[156:159], v[196:199], v[70:73]
	v_mfma_f32_16x16x32_bf16 v[66:69], v[164:167], v[196:199], v[66:69]
	v_mfma_f32_16x16x32_bf16 v[118:121], v[160:163], v[176:179], v[118:121]
	v_mfma_f32_16x16x32_bf16 v[110:113], v[168:171], v[176:179], v[110:113]
	v_mfma_f32_16x16x32_bf16 v[102:105], v[160:163], v[184:187], v[102:105]
	v_mfma_f32_16x16x32_bf16 v[94:97], v[168:171], v[184:187], v[94:97]
	v_mfma_f32_16x16x32_bf16 v[86:89], v[160:163], v[192:195], v[86:89]
	v_mfma_f32_16x16x32_bf16 v[78:81], v[168:171], v[192:195], v[78:81]
	v_mfma_f32_16x16x32_bf16 v[70:73], v[160:163], v[200:203], v[70:73]
	v_mfma_f32_16x16x32_bf16 v[66:69], v[168:171], v[200:203], v[66:69]
	s_barrier
	s_mov_b32 m0, s24
	s_mov_b32 s10, s6
	s_mov_b32 s11, s7
	ds_read_b128 v[172:175], v139 offset:16384
	ds_read_b128 v[176:179], v139 offset:17408
	ds_read_b128 v[180:183], v139 offset:18432
	ds_read_b128 v[184:187], v139 offset:19456
	ds_read_b128 v[188:191], v139 offset:20480
	ds_read_b128 v[192:195], v139 offset:21504
	ds_read_b128 v[196:199], v139 offset:22528
	ds_read_b128 v[200:203], v139 offset:23552
	buffer_load_dwordx4 v135, s[8:11], s52 offen lds
	s_mov_b32 m0, s26
	s_add_i32 s54, s52, 0x200000
	buffer_load_dwordx4 v137, s[8:11], s52 offen lds
	s_mov_b32 m0, s27
	s_nop 0
	buffer_load_dwordx4 v135, s[8:11], s54 offen lds
	s_mov_b32 m0, s28
	s_nop 0
	buffer_load_dwordx4 v137, s[8:11], s54 offen lds
	s_mov_b32 m0, s23
	s_nop 0
	buffer_load_dwordx4 v134, s[4:7], s53 offen lds
	s_mov_b32 m0, s29
	s_nop 0
	buffer_load_dwordx4 v136, s[4:7], s53 offen lds
	s_waitcnt vmcnt(8)
	s_waitcnt lgkmcnt(0)
	s_barrier
	s_waitcnt lgkmcnt(7)
	v_mfma_f32_16x16x32_bf16 v[62:65], v[140:143], v[172:175], v[62:65]
	v_mfma_f32_16x16x32_bf16 v[58:61], v[148:151], v[172:175], v[58:61]
	s_waitcnt lgkmcnt(5)
	v_mfma_f32_16x16x32_bf16 v[50:53], v[140:143], v[180:183], v[50:53]
	v_mfma_f32_16x16x32_bf16 v[42:45], v[148:151], v[180:183], v[42:45]
	s_waitcnt lgkmcnt(3)
	v_mfma_f32_16x16x32_bf16 v[34:37], v[140:143], v[188:191], v[34:37]
	v_mfma_f32_16x16x32_bf16 v[26:29], v[148:151], v[188:191], v[26:29]
	s_waitcnt lgkmcnt(1)
	v_mfma_f32_16x16x32_bf16 v[18:21], v[140:143], v[196:199], v[18:21]
	v_mfma_f32_16x16x32_bf16 v[10:13], v[148:151], v[196:199], v[10:13]
	v_mfma_f32_16x16x32_bf16 v[62:65], v[144:147], v[176:179], v[62:65]
	v_mfma_f32_16x16x32_bf16 v[58:61], v[152:155], v[176:179], v[58:61]
	v_mfma_f32_16x16x32_bf16 v[50:53], v[144:147], v[184:187], v[50:53]
	v_mfma_f32_16x16x32_bf16 v[42:45], v[152:155], v[184:187], v[42:45]
	v_mfma_f32_16x16x32_bf16 v[34:37], v[144:147], v[192:195], v[34:37]
	v_mfma_f32_16x16x32_bf16 v[26:29], v[152:155], v[192:195], v[26:29]
	s_waitcnt lgkmcnt(0)
	v_mfma_f32_16x16x32_bf16 v[18:21], v[144:147], v[200:203], v[18:21]
	v_mfma_f32_16x16x32_bf16 v[10:13], v[152:155], v[200:203], v[10:13]
	v_mfma_f32_16x16x32_bf16 v[54:57], v[156:159], v[172:175], v[54:57]
	v_mfma_f32_16x16x32_bf16 v[46:49], v[164:167], v[172:175], v[46:49]
	v_mfma_f32_16x16x32_bf16 v[38:41], v[156:159], v[180:183], v[38:41]
	v_mfma_f32_16x16x32_bf16 v[30:33], v[164:167], v[180:183], v[30:33]
	v_mfma_f32_16x16x32_bf16 v[22:25], v[156:159], v[188:191], v[22:25]
	v_mfma_f32_16x16x32_bf16 v[14:17], v[164:167], v[188:191], v[14:17]
	v_mfma_f32_16x16x32_bf16 v[6:9], v[156:159], v[196:199], v[6:9]
	v_mfma_f32_16x16x32_bf16 v[2:5], v[164:167], v[196:199], v[2:5]
	v_mfma_f32_16x16x32_bf16 v[54:57], v[160:163], v[176:179], v[54:57]
	v_mfma_f32_16x16x32_bf16 v[46:49], v[168:171], v[176:179], v[46:49]
	v_mfma_f32_16x16x32_bf16 v[38:41], v[160:163], v[184:187], v[38:41]
	v_mfma_f32_16x16x32_bf16 v[30:33], v[168:171], v[184:187], v[30:33]
	v_mfma_f32_16x16x32_bf16 v[22:25], v[160:163], v[192:195], v[22:25]
	v_mfma_f32_16x16x32_bf16 v[14:17], v[168:171], v[192:195], v[14:17]
	v_mfma_f32_16x16x32_bf16 v[6:9], v[160:163], v[200:203], v[6:9]
	v_mfma_f32_16x16x32_bf16 v[2:5], v[168:171], v[200:203], v[2:5]
	s_barrier
	v_add_u32_e32 v152, 0x18000, v138
	v_add_u32_e32 v168, 0x1c000, v138
	ds_read_b128 v[140:143], v152
	ds_read_b128 v[144:147], v152 offset:1024
	ds_read_b128 v[148:151], v152 offset:2048
	ds_read_b128 v[152:155], v152 offset:3072
	ds_read_b128 v[156:159], v168
	ds_read_b128 v[160:163], v168 offset:1024
	ds_read_b128 v[164:167], v168 offset:2048
	ds_read_b128 v[168:171], v168 offset:3072
	s_add_i32 s53, s53, 0x200000
	s_mov_b32 m0, s31
	ds_read_b128 v[172:175], v139 offset:32768
	ds_read_b128 v[176:179], v139 offset:33792
	ds_read_b128 v[180:183], v139 offset:34816
	ds_read_b128 v[184:187], v139 offset:35840
	ds_read_b128 v[188:191], v139 offset:36864
	ds_read_b128 v[192:195], v139 offset:37888
	ds_read_b128 v[196:199], v139 offset:38912
	ds_read_b128 v[200:203], v139 offset:39936
	buffer_load_dwordx4 v134, s[4:7], s53 offen lds
	s_mov_b32 m0, s33
	s_nop 0
	buffer_load_dwordx4 v136, s[4:7], s53 offen lds
	s_waitcnt vmcnt(8)
	s_waitcnt lgkmcnt(0)
	s_barrier
	s_waitcnt lgkmcnt(7)
	v_mfma_f32_16x16x32_bf16 v[126:129], v[140:143], v[172:175], v[126:129]
	v_mfma_f32_16x16x32_bf16 v[122:125], v[148:151], v[172:175], v[122:125]
	s_waitcnt lgkmcnt(5)
	v_mfma_f32_16x16x32_bf16 v[114:117], v[140:143], v[180:183], v[114:117]
	v_mfma_f32_16x16x32_bf16 v[106:109], v[148:151], v[180:183], v[106:109]
	s_waitcnt lgkmcnt(3)
	v_mfma_f32_16x16x32_bf16 v[98:101], v[140:143], v[188:191], v[98:101]
	v_mfma_f32_16x16x32_bf16 v[90:93], v[148:151], v[188:191], v[90:93]
	s_waitcnt lgkmcnt(1)
	v_mfma_f32_16x16x32_bf16 v[82:85], v[140:143], v[196:199], v[82:85]
	v_mfma_f32_16x16x32_bf16 v[74:77], v[148:151], v[196:199], v[74:77]
	v_mfma_f32_16x16x32_bf16 v[126:129], v[144:147], v[176:179], v[126:129]
	v_mfma_f32_16x16x32_bf16 v[122:125], v[152:155], v[176:179], v[122:125]
	v_mfma_f32_16x16x32_bf16 v[114:117], v[144:147], v[184:187], v[114:117]
	v_mfma_f32_16x16x32_bf16 v[106:109], v[152:155], v[184:187], v[106:109]
	v_mfma_f32_16x16x32_bf16 v[98:101], v[144:147], v[192:195], v[98:101]
	v_mfma_f32_16x16x32_bf16 v[90:93], v[152:155], v[192:195], v[90:93]
	s_waitcnt lgkmcnt(0)
	v_mfma_f32_16x16x32_bf16 v[82:85], v[144:147], v[200:203], v[82:85]
	v_mfma_f32_16x16x32_bf16 v[74:77], v[152:155], v[200:203], v[74:77]
	v_mfma_f32_16x16x32_bf16 v[118:121], v[156:159], v[172:175], v[118:121]
	v_mfma_f32_16x16x32_bf16 v[110:113], v[164:167], v[172:175], v[110:113]
	v_mfma_f32_16x16x32_bf16 v[102:105], v[156:159], v[180:183], v[102:105]
	v_mfma_f32_16x16x32_bf16 v[94:97], v[164:167], v[180:183], v[94:97]
	v_mfma_f32_16x16x32_bf16 v[86:89], v[156:159], v[188:191], v[86:89]
	v_mfma_f32_16x16x32_bf16 v[78:81], v[164:167], v[188:191], v[78:81]
	v_mfma_f32_16x16x32_bf16 v[70:73], v[156:159], v[196:199], v[70:73]
	v_mfma_f32_16x16x32_bf16 v[66:69], v[164:167], v[196:199], v[66:69]
	v_mfma_f32_16x16x32_bf16 v[118:121], v[160:163], v[176:179], v[118:121]
	v_mfma_f32_16x16x32_bf16 v[110:113], v[168:171], v[176:179], v[110:113]
	v_mfma_f32_16x16x32_bf16 v[102:105], v[160:163], v[184:187], v[102:105]
	v_mfma_f32_16x16x32_bf16 v[94:97], v[168:171], v[184:187], v[94:97]
	v_mfma_f32_16x16x32_bf16 v[86:89], v[160:163], v[192:195], v[86:89]
	v_mfma_f32_16x16x32_bf16 v[78:81], v[168:171], v[192:195], v[78:81]
	v_mfma_f32_16x16x32_bf16 v[70:73], v[160:163], v[200:203], v[70:73]
	v_mfma_f32_16x16x32_bf16 v[66:69], v[168:171], v[200:203], v[66:69]
	s_barrier
	s_mov_b32 m0, s34
	s_or_b32 s53, s52, 0x80
	ds_read_b128 v[172:175], v139 offset:49152
	ds_read_b128 v[176:179], v139 offset:50176
	ds_read_b128 v[180:183], v139 offset:51200
	ds_read_b128 v[184:187], v139 offset:52224
	ds_read_b128 v[188:191], v139 offset:53248
	ds_read_b128 v[192:195], v139 offset:54272
	ds_read_b128 v[196:199], v139 offset:55296
	ds_read_b128 v[200:203], v139 offset:56320
	buffer_load_dwordx4 v135, s[8:11], s53 offen lds
	s_mov_b32 m0, s35
	s_add_i32 s52, s52, 0x200080
	buffer_load_dwordx4 v137, s[8:11], s53 offen lds
	s_mov_b32 m0, s39
	s_nop 0
	buffer_load_dwordx4 v135, s[8:11], s52 offen lds
	s_mov_b32 m0, s40
	s_nop 0
	buffer_load_dwordx4 v137, s[8:11], s52 offen lds
	s_mov_b32 m0, s37
	s_nop 0
	buffer_load_dwordx4 v134, s[4:7], s51 offen lds
	s_mov_b32 m0, s38
	s_nop 0
	buffer_load_dwordx4 v136, s[4:7], s51 offen lds
	s_waitcnt vmcnt(8)
	s_waitcnt lgkmcnt(0)
	s_barrier
	s_waitcnt lgkmcnt(7)
	v_mfma_f32_16x16x32_bf16 v[62:65], v[140:143], v[172:175], v[62:65]
	v_mfma_f32_16x16x32_bf16 v[58:61], v[148:151], v[172:175], v[58:61]
	s_waitcnt lgkmcnt(5)
	v_mfma_f32_16x16x32_bf16 v[50:53], v[140:143], v[180:183], v[50:53]
	v_mfma_f32_16x16x32_bf16 v[42:45], v[148:151], v[180:183], v[42:45]
	s_waitcnt lgkmcnt(3)
	v_mfma_f32_16x16x32_bf16 v[34:37], v[140:143], v[188:191], v[34:37]
	v_mfma_f32_16x16x32_bf16 v[26:29], v[148:151], v[188:191], v[26:29]
	s_waitcnt lgkmcnt(1)
	v_mfma_f32_16x16x32_bf16 v[18:21], v[140:143], v[196:199], v[18:21]
	v_mfma_f32_16x16x32_bf16 v[10:13], v[148:151], v[196:199], v[10:13]
	v_mfma_f32_16x16x32_bf16 v[62:65], v[144:147], v[176:179], v[62:65]
	v_mfma_f32_16x16x32_bf16 v[58:61], v[152:155], v[176:179], v[58:61]
	v_mfma_f32_16x16x32_bf16 v[50:53], v[144:147], v[184:187], v[50:53]
	v_mfma_f32_16x16x32_bf16 v[42:45], v[152:155], v[184:187], v[42:45]
	v_mfma_f32_16x16x32_bf16 v[34:37], v[144:147], v[192:195], v[34:37]
	v_mfma_f32_16x16x32_bf16 v[26:29], v[152:155], v[192:195], v[26:29]
	s_waitcnt lgkmcnt(0)
	v_mfma_f32_16x16x32_bf16 v[18:21], v[144:147], v[200:203], v[18:21]
	v_mfma_f32_16x16x32_bf16 v[10:13], v[152:155], v[200:203], v[10:13]
	v_mfma_f32_16x16x32_bf16 v[54:57], v[156:159], v[172:175], v[54:57]
	v_mfma_f32_16x16x32_bf16 v[46:49], v[164:167], v[172:175], v[46:49]
	v_mfma_f32_16x16x32_bf16 v[38:41], v[156:159], v[180:183], v[38:41]
	v_mfma_f32_16x16x32_bf16 v[30:33], v[164:167], v[180:183], v[30:33]
	v_mfma_f32_16x16x32_bf16 v[22:25], v[156:159], v[188:191], v[22:25]
	v_mfma_f32_16x16x32_bf16 v[14:17], v[164:167], v[188:191], v[14:17]
	v_mfma_f32_16x16x32_bf16 v[6:9], v[156:159], v[196:199], v[6:9]
	v_mfma_f32_16x16x32_bf16 v[2:5], v[164:167], v[196:199], v[2:5]
	v_mfma_f32_16x16x32_bf16 v[54:57], v[160:163], v[176:179], v[54:57]
	v_mfma_f32_16x16x32_bf16 v[46:49], v[168:171], v[176:179], v[46:49]
	v_mfma_f32_16x16x32_bf16 v[38:41], v[160:163], v[184:187], v[38:41]
	v_mfma_f32_16x16x32_bf16 v[30:33], v[168:171], v[184:187], v[30:33]
	v_mfma_f32_16x16x32_bf16 v[22:25], v[160:163], v[192:195], v[22:25]
	v_mfma_f32_16x16x32_bf16 v[14:17], v[168:171], v[192:195], v[14:17]
	v_mfma_f32_16x16x32_bf16 v[6:9], v[160:163], v[200:203], v[6:9]
	v_mfma_f32_16x16x32_bf16 v[2:5], v[168:171], v[200:203], v[2:5]
	s_barrier
	s_add_i32 s49, s49, 2
	s_addk_i32 s50, 0x100
	s_cmpk_gt_u32 s49, 0x7d
	s_cbranch_scc0 .LBB0_1029
	s_andn2_b64 vcc, exec, s[2:3]
	s_cbranch_vccnz .LBB0_1021
	v_mov_b32_e32 v2, 0
	s_mov_b32 s17, s44
	s_mov_b32 s14, s45
	s_mov_b32 s25, s46
	s_mov_b32 s30, s13
	s_mov_b32 s43, s12
	v_mov_b32_e32 v3, v2
	v_mov_b32_e32 v4, v2
	v_mov_b32_e32 v5, v2
	v_mov_b32_e32 v6, v2
	v_mov_b32_e32 v7, v2
	v_mov_b32_e32 v8, v2
	v_mov_b32_e32 v9, v2
	v_mov_b32_e32 v14, v2
	v_mov_b32_e32 v15, v2
	v_mov_b32_e32 v16, v2
	v_mov_b32_e32 v17, v2
	v_mov_b32_e32 v22, v2
	v_mov_b32_e32 v23, v2
	v_mov_b32_e32 v24, v2
	v_mov_b32_e32 v25, v2
	v_mov_b32_e32 v30, v2
	v_mov_b32_e32 v31, v2
	v_mov_b32_e32 v32, v2
	v_mov_b32_e32 v33, v2
	v_mov_b32_e32 v38, v2
	v_mov_b32_e32 v39, v2
	v_mov_b32_e32 v40, v2
	v_mov_b32_e32 v41, v2
	v_mov_b32_e32 v46, v2
	v_mov_b32_e32 v47, v2
	v_mov_b32_e32 v48, v2
	v_mov_b32_e32 v49, v2
	v_mov_b32_e32 v54, v2
	v_mov_b32_e32 v55, v2
	v_mov_b32_e32 v56, v2
	v_mov_b32_e32 v57, v2
	v_mov_b32_e32 v10, v2
	v_mov_b32_e32 v11, v2
	v_mov_b32_e32 v12, v2
	v_mov_b32_e32 v13, v2
	v_mov_b32_e32 v18, v2
	v_mov_b32_e32 v19, v2
	v_mov_b32_e32 v20, v2
	v_mov_b32_e32 v21, v2
	v_mov_b32_e32 v26, v2
	v_mov_b32_e32 v27, v2
	v_mov_b32_e32 v28, v2
	v_mov_b32_e32 v29, v2
	v_mov_b32_e32 v34, v2
	v_mov_b32_e32 v35, v2
	v_mov_b32_e32 v36, v2
	v_mov_b32_e32 v37, v2
	v_mov_b32_e32 v42, v2
	v_mov_b32_e32 v43, v2
	v_mov_b32_e32 v44, v2
	v_mov_b32_e32 v45, v2
	v_mov_b32_e32 v50, v2
	v_mov_b32_e32 v51, v2
	v_mov_b32_e32 v52, v2
	v_mov_b32_e32 v53, v2
	v_mov_b32_e32 v58, v2
	v_mov_b32_e32 v59, v2
	v_mov_b32_e32 v60, v2
	v_mov_b32_e32 v61, v2
	v_mov_b32_e32 v62, v2
	v_mov_b32_e32 v63, v2
	v_mov_b32_e32 v64, v2
	v_mov_b32_e32 v65, v2
	v_mov_b32_e32 v66, v2
	v_mov_b32_e32 v67, v2
	v_mov_b32_e32 v68, v2
	v_mov_b32_e32 v69, v2
	v_mov_b32_e32 v70, v2
	v_mov_b32_e32 v71, v2
	v_mov_b32_e32 v72, v2
	v_mov_b32_e32 v73, v2
	v_mov_b32_e32 v78, v2
	v_mov_b32_e32 v79, v2
	v_mov_b32_e32 v80, v2
	v_mov_b32_e32 v81, v2
	v_mov_b32_e32 v86, v2
	v_mov_b32_e32 v87, v2
	v_mov_b32_e32 v88, v2
	v_mov_b32_e32 v89, v2
	v_mov_b32_e32 v94, v2
	v_mov_b32_e32 v95, v2
	v_mov_b32_e32 v96, v2
	v_mov_b32_e32 v97, v2
	v_mov_b32_e32 v102, v2
	v_mov_b32_e32 v103, v2
	v_mov_b32_e32 v104, v2
	v_mov_b32_e32 v105, v2
	v_mov_b32_e32 v110, v2
	v_mov_b32_e32 v111, v2
	v_mov_b32_e32 v112, v2
	v_mov_b32_e32 v113, v2
	v_mov_b32_e32 v118, v2
	v_mov_b32_e32 v119, v2
	v_mov_b32_e32 v120, v2
	v_mov_b32_e32 v121, v2
	v_mov_b32_e32 v74, v2
	v_mov_b32_e32 v75, v2
	v_mov_b32_e32 v76, v2
	v_mov_b32_e32 v77, v2
	v_mov_b32_e32 v82, v2
	v_mov_b32_e32 v83, v2
	v_mov_b32_e32 v84, v2
	v_mov_b32_e32 v85, v2
	v_mov_b32_e32 v90, v2
	v_mov_b32_e32 v91, v2
	v_mov_b32_e32 v92, v2
	v_mov_b32_e32 v93, v2
	v_mov_b32_e32 v98, v2
	v_mov_b32_e32 v99, v2
	v_mov_b32_e32 v100, v2
	v_mov_b32_e32 v101, v2
	v_mov_b32_e32 v106, v2
	v_mov_b32_e32 v107, v2
	v_mov_b32_e32 v108, v2
	v_mov_b32_e32 v109, v2
	v_mov_b32_e32 v114, v2
	v_mov_b32_e32 v115, v2
	v_mov_b32_e32 v116, v2
	v_mov_b32_e32 v117, v2
	v_mov_b32_e32 v122, v2
	v_mov_b32_e32 v123, v2
	v_mov_b32_e32 v124, v2
	v_mov_b32_e32 v125, v2
	v_mov_b32_e32 v126, v2
	v_mov_b32_e32 v127, v2
	v_mov_b32_e32 v128, v2
	v_mov_b32_e32 v129, v2
	s_branch .LBB0_1021
